# v_N plus saddr-form LDS-DMA in P1/P4/P8 K-loops, P14 saddr + 4/4 stage rebalance, MoBA row-max via permlane swaps, P0 dispatch chain cut short
# speedup vs baseline: 1.0100x; 1.0041x over previous
.Lp0_body:
	ds_write2_b32 v62, v200, v201 offset1:1
	ds_write2_b32 v62, v202, v203 offset0:2 offset1:3
	ds_write2_b32 v70, v204, v205 offset1:1
	ds_write2_b32 v71, v206, v207 offset1:1
	ds_write2_b32 v72, v208, v209 offset1:1
	ds_write2_b32 v73, v210, v211 offset1:1
	ds_write2_b32 v74, v212, v213 offset1:1
	ds_write2_b32 v75, v214, v215 offset1:1
	ds_write2_b32 v76, v216, v217 offset1:1
	ds_write2_b32 v77, v218, v219 offset1:1
	ds_write2_b32 v78, v220, v221 offset1:1
	ds_write2_b32 v79, v222, v223 offset1:1
	ds_write2_b32 v80, v224, v225 offset1:1
	ds_write2_b32 v81, v226, v227 offset1:1
	ds_write2_b32 v82, v228, v229 offset1:1
	ds_write2_b32 v83, v230, v231 offset1:1
	v_mov_b32_e32 v234, v232
	v_mov_b32_e32 v235, v233
	s_add_i32 s98, s3, s92
	s_cmp_gt_i32 s98, 0x28bff
	s_cselect_b32 s98, s3, s98
	v_readlane_b32 s100, v246, 3
	v_readlane_b32 s101, v246, 4
	s_mov_b32 s76, 0
	s_mov_b32 s77, 16
	s_mov_b32 s78, 0x158
	s_mov_b32 s79, 0xbe83
	s_mov_b32 s80, 0
	s_mov_b32 s81, 0x158
	s_mov_b64 s[82:83], s[28:29]
	s_cmp_ge_u32 s98, 0x5600
	s_cselect_b32 s76, 0x5600, s76
	s_cselect_b32 s77, 18, s77
	s_cselect_b64 s[82:83], s[4:5], s[82:83]
	s_cmp_ge_u32 s98, 0xac00
	s_cselect_b32 s76, 0xac00, s76
	s_cselect_b32 s77, 20, s77
	s_cselect_b32 s78, 0x80, s78
	s_cselect_b32 s79, 0x20000, s79
	s_cselect_b32 s81, 0x80, s81
	s_cmp_ge_u32 s98, 0x10200
	s_cselect_b32 s76, 0x10200, s76
	s_cselect_b32 s77, 24, s77
	s_cselect_b32 s78, 0x120, s78
	s_cselect_b32 s79, 0xe38f, s79
	s_cselect_b32 s81, 0x120, s81
	s_cselect_b64 s[82:83], s[90:91], s[82:83]
	s_cmp_ge_u32 s98, 0x14a00
	s_cselect_b32 s76, 0x14a00, s76
	s_cselect_b32 s77, 34, s77
	s_cselect_b32 s78, 0x80, s78
	s_cselect_b32 s79, 0x20000, s79
	s_cselect_b32 s81, 0x80, s81
	s_cselect_b64 s[82:83], s[100:101], s[82:83]
	s_cmp_ge_u32 s98, 0x16a00
	s_cselect_b32 s76, 0x16a00, s76
	s_cselect_b32 s77, 24, s77
	s_cselect_b32 s78, 64, s78
	s_cselect_b32 s79, 0x40000, s79
	s_cselect_b32 s80, 64, s80
	s_cselect_b32 s81, 0x120, s81
	s_cmp_ge_u32 s98, 0x17a00
	s_cselect_b32 s76, 0x17a00, s76
	s_cselect_b32 s77, 43, s77
	s_cselect_b32 s78, 16, s78
	s_cselect_b32 s79, 0x100000, s79
	s_cselect_b32 s80, 0, s80
	s_cselect_b32 s81, 16, s81
	s_cmp_ge_u32 s98, 0x17e00
	s_cselect_b32 s76, 0x17e00, s76
	s_cselect_b32 s77, 45, s77
	s_cmp_ge_u32 s98, 0x18200
	s_cselect_b32 s76, 0x18200, s76
	s_cselect_b32 s77, 47, s77
	s_cmp_ge_u32 s98, 0x18600
	s_cselect_b32 s76, 0x18600, s76
	s_cselect_b32 s77, 49, s77
	s_cselect_b32 s78, 0x80, s78
	s_cselect_b32 s79, 0x20000, s79
	s_cselect_b32 s81, 0x80, s81
	s_cmp_ge_u32 s98, 0x18a00
	s_cselect_b32 s76, 0x18a00, s76
	s_cselect_b32 s77, 53, s77
	s_cselect_b32 s78, 0x158, s78
	s_cselect_b32 s79, 0xbe83, s79
	s_cselect_b32 s81, 0x158, s81
	s_cmp_ge_u32 s98, 0x1e000
	s_cselect_b32 s76, 0x1e000, s76
	s_cselect_b32 s77, 55, s77
	s_cmp_ge_u32 s98, 0x23600
	s_cselect_b32 s76, 0x23600, s76
	s_cselect_b32 s77, 2, s77
	s_cselect_b32 s78, 0x80, s78
	s_cselect_b32 s79, 0x20000, s79
	s_cselect_b32 s81, 0x80, s81
	s_sub_u32 s98, s98, s76
	s_mul_i32 s99, s98, s79
	s_lshr_b32 s99, s99, 24
	s_mul_i32 s76, s99, s78
	s_sub_u32 s98, s98, s76
	s_lshl_b32 s79, s98, 7
	s_add_u32 s98, s98, s80
	s_lshl_b32 s98, s98, 7
	s_mul_i32 s99, s99, s81
	s_lshl_b32 s99, s99, 13
	s_add_u32 s98, s98, s99
	s_add_i32 s78, s77, 1
	s_lshl_b32 s81, s81, 7
	s_nop 3
	v_readlane_b32 s100, v247, s77
	v_readlane_b32 s101, v247, s78
	v_mad_u32_u24 v252, v35, s81, v2
	v_lshl_add_u32 v251, v63, 2, s79
	s_lshl_b32 s81, s81, 3
	s_add_u32 s100, s100, s98
	s_addc_u32 s101, s101, 0
	global_load_dword v232, v251, s[82:83]
	global_load_dword v233, v251, s[82:83] offset:64
	global_load_dwordx4 v[200:203], v252, s[100:101]
	s_add_u32 s100, s100, s81
	s_addc_u32 s101, s101, 0
	global_load_dwordx4 v[204:207], v252, s[100:101]
	s_add_u32 s100, s100, s81
	s_addc_u32 s101, s101, 0
	global_load_dwordx4 v[208:211], v252, s[100:101]
	s_add_u32 s100, s100, s81
	s_addc_u32 s101, s101, 0
	global_load_dwordx4 v[212:215], v252, s[100:101]
	s_add_u32 s100, s100, s81
	s_addc_u32 s101, s101, 0
	global_load_dwordx4 v[216:219], v252, s[100:101]
	s_add_u32 s100, s100, s81
	s_addc_u32 s101, s101, 0
	global_load_dwordx4 v[220:223], v252, s[100:101]
	s_add_u32 s100, s100, s81
	s_addc_u32 s101, s101, 0
	global_load_dwordx4 v[224:227], v252, s[100:101]
	s_add_u32 s100, s100, s81
	s_addc_u32 s101, s101, 0
	global_load_dwordx4 v[228:231], v252, s[100:101]
	s_cmpk_gt_i32 s3, 0x55ff
	s_mov_b64 s[0:1], -1
	s_cbranch_scc0 .LBB0_134
	s_cmpk_gt_u32 s3, 0xabff
	s_cbranch_scc0 .LBB0_131
	s_cmp_gt_u32 s3, 0x101ff
	s_cbranch_scc0 .LBB0_128
	s_cmp_gt_u32 s3, 0x149ff
	s_cbranch_scc0 .LBB0_125
	s_cmp_gt_u32 s3, 0x169ff
	s_cbranch_scc0 .LBB0_122
	s_cmp_gt_u32 s3, 0x179ff
	s_cbranch_scc0 .LBB0_119
	s_cmp_gt_u32 s3, 0x17dff
	s_cbranch_scc0 .LBB0_116
	s_cmp_gt_u32 s3, 0x181ff
	s_cbranch_scc0 .LBB0_113
	s_cmp_gt_u32 s3, 0x185ff
	s_cbranch_scc0 .LBB0_110
	s_cmp_gt_u32 s3, 0x189ff
	s_cbranch_scc0 .LBB0_107
	s_cmp_gt_u32 s3, 0x1dfff
	s_cbranch_scc0 .LBB0_104
	s_cmp_gt_u32 s3, 0x235ff
	s_cbranch_scc0 .LBB0_101
	s_add_i32 s0, s3, 0xca00
	s_lshr_b32 s0, s0, 1
	s_and_b32 s0, s0, 0x7fc0
	s_lshl_b32 s1, s3, 5
	v_or_b32_e32 v24, s0, v35
	v_readlane_b32 s36, v247, 2
	s_and_b32 s7, s1, 0xfe0
	v_lshlrev_b32_e32 v24, 14, v24
	v_mov_b32_e32 v25, v3
	v_readlane_b32 s37, v247, 3
	s_lshl_b32 s10, s7, 2
	v_mov_b32_e32 v94, v3
	v_lshl_add_u64 v[24:25], s[36:37], 0, v[24:25]
	v_lshl_add_u64 v[24:25], v[24:25], 0, s[10:11]
	v_lshl_add_u64 v[32:33], v[24:25], 0, v[2:3]
	v_add_co_u32_e32 v28, vcc, s18, v32
	v_mov_b32_e32 v95, v3
	s_nop 0
	v_addc_co_u32_e32 v29, vcc, 0, v33, vcc
	v_add_co_u32_e32 v36, vcc, s19, v32
	s_nop 0
	v_addc_co_u32_e32 v37, vcc, 0, v33, vcc
	v_add_co_u32_e32 v40, vcc, s20, v32
	v_mov_b32_e32 v96, v3
	s_nop 0
	v_addc_co_u32_e32 v41, vcc, 0, v33, vcc
	v_add_co_u32_e32 v44, vcc, s21, v32
	s_nop 0
	v_addc_co_u32_e32 v45, vcc, 0, v33, vcc
	v_add_co_u32_e32 v48, vcc, s30, v32
	v_mov_b32_e32 v97, v3
	s_nop 0
	v_addc_co_u32_e32 v49, vcc, 0, v33, vcc
	s_nop 0
	v_add_co_u32_e32 v52, vcc, s31, v32
	s_mov_b32 s1, s11
	s_nop 0
	v_addc_co_u32_e32 v53, vcc, 0, v33, vcc
	v_add_co_u32_e32 v32, vcc, s34, v32
	v_mov_b32_e32 v61, v3
	s_nop 0
	v_addc_co_u32_e32 v33, vcc, 0, v33, vcc
	v_lshl_add_u64 v[32:33], v[4:5], 0, s[0:1]
	v_readlane_b32 s38, v247, 4
	v_readlane_b32 s39, v247, 5
	s_mov_b64 s[0:1], 0
	s_waitcnt lgkmcnt(0)
	ds_read2_b32 v[24:25], v64 offset1:16
	ds_read2_b32 v[26:27], v64 offset0:33 offset1:49
	ds_read2_b32 v[28:29], v64 offset0:66 offset1:82
	ds_read2_b32 v[30:31], v64 offset0:99 offset1:115
	ds_read2_b32 v[36:37], v64 offset0:132 offset1:148
	ds_read2_b32 v[38:39], v64 offset0:165 offset1:181
	ds_read2_b32 v[40:41], v64 offset0:198 offset1:214
	ds_read2_b32 v[42:43], v64 offset0:231 offset1:247
	ds_read2_b32 v[44:45], v85 offset0:8 offset1:24
	ds_read2_b32 v[46:47], v85 offset0:41 offset1:57
	ds_read2_b32 v[48:49], v85 offset0:74 offset1:90
	ds_read2_b32 v[50:51], v85 offset0:107 offset1:123
	s_waitcnt lgkmcnt(11)
	v_mul_f32_e32 v24, 0x43000000, v24
	s_waitcnt lgkmcnt(10)
	v_mul_f32_e32 v26, 0x43000000, v26
	s_waitcnt lgkmcnt(7)
	v_mul_f32_e32 v36, 0x43000000, v36
	s_waitcnt lgkmcnt(6)
	v_mul_f32_e32 v38, 0x43000000, v38
	v_med3_f32 v24, v24, s35, v84
	v_med3_f32 v26, v26, s35, v84
	v_med3_f32 v36, v36, s35, v84
	v_med3_f32 v38, v38, s35, v84
	v_cvt_pk_fp8_f32 v94, v24, v26
	v_cvt_pk_fp8_f32 v95, v36, v38
	v_mul_f32_e32 v28, 0x43000000, v28
	v_mul_f32_e32 v30, 0x43000000, v30
	s_waitcnt lgkmcnt(5)
	v_mul_f32_e32 v40, 0x43000000, v40
	s_waitcnt lgkmcnt(4)
	v_mul_f32_e32 v42, 0x43000000, v42
	s_waitcnt lgkmcnt(3)
	v_mul_f32_e32 v44, 0x43000000, v44
	s_waitcnt lgkmcnt(2)
	v_mul_f32_e32 v46, 0x43000000, v46
	v_med3_f32 v28, v28, s35, v84
	v_med3_f32 v30, v30, s35, v84
	v_med3_f32 v24, v40, s35, v84
	v_med3_f32 v26, v42, s35, v84
	v_cvt_pk_fp8_f32 v94, v28, v30 op_sel:[0,0,1]
	v_cvt_pk_fp8_f32 v95, v24, v26 op_sel:[0,0,1]
	v_med3_f32 v26, v44, s35, v84
	v_med3_f32 v28, v46, s35, v84
	v_cvt_pk_fp8_f32 v96, v26, v28
	ds_read2_b32 v[52:53], v85 offset0:140 offset1:156
	ds_read2_b32 v[54:55], v85 offset0:173 offset1:189
	ds_read2_b32 v[56:57], v85 offset0:206 offset1:222
	s_waitcnt lgkmcnt(4)
	v_mul_f32_e32 v48, 0x43000000, v48
	s_waitcnt lgkmcnt(3)
	v_mul_f32_e32 v24, 0x43000000, v50
	v_med3_f32 v26, v48, s35, v84
	v_med3_f32 v24, v24, s35, v84
	ds_read2_b32 v[58:59], v85 offset0:239 offset1:255
	v_cvt_pk_fp8_f32 v96, v26, v24 op_sel:[0,0,1]
	s_waitcnt lgkmcnt(3)
	v_mul_f32_e32 v24, 0x43000000, v52
	s_waitcnt lgkmcnt(2)
	v_mul_f32_e32 v26, 0x43000000, v54
	v_med3_f32 v24, v24, s35, v84
	v_med3_f32 v26, v26, s35, v84
	v_cvt_pk_fp8_f32 v97, v24, v26
	s_waitcnt lgkmcnt(1)
	v_mul_f32_e32 v28, 0x43000000, v56
	s_waitcnt lgkmcnt(0)
	v_mul_f32_e32 v24, 0x43000000, v58
	v_med3_f32 v26, v28, s35, v84
	v_med3_f32 v24, v24, s35, v84
	v_cvt_pk_fp8_f32 v97, v26, v24 op_sel:[0,0,1]
	v_or_b32_e32 v24, s7, v63
	v_mul_u32_u24_e32 v60, 0x2b00, v24
	v_mul_f32_e32 v24, 0x43000000, v25
	v_mul_f32_e32 v25, 0x43000000, v27
	v_med3_f32 v27, v24, s35, v84
	v_med3_f32 v25, v25, s35, v84
	v_mov_b32_e32 v24, v3
	v_cvt_pk_fp8_f32 v24, v27, v25
	v_mul_f32_e32 v26, 0x43000000, v29
	v_mul_f32_e32 v25, 0x43000000, v31
	v_med3_f32 v26, v26, s35, v84
	v_med3_f32 v25, v25, s35, v84
	v_cvt_pk_fp8_f32 v24, v26, v25 op_sel:[0,0,1]
	v_mul_f32_e32 v25, 0x43000000, v37
	v_mul_f32_e32 v26, 0x43000000, v39
	v_med3_f32 v28, v25, s35, v84
	v_med3_f32 v26, v26, s35, v84
	v_mov_b32_e32 v25, v3
	v_cvt_pk_fp8_f32 v25, v28, v26
	v_mul_f32_e32 v27, 0x43000000, v41
	v_mul_f32_e32 v26, 0x43000000, v43
	v_med3_f32 v27, v27, s35, v84
	v_med3_f32 v26, v26, s35, v84
	v_cvt_pk_fp8_f32 v25, v27, v26 op_sel:[0,0,1]
	v_mul_f32_e32 v26, 0x43000000, v45
	v_mul_f32_e32 v27, 0x43000000, v47
	v_med3_f32 v29, v26, s35, v84
	v_med3_f32 v27, v27, s35, v84
	v_mov_b32_e32 v26, v3
	v_cvt_pk_fp8_f32 v26, v29, v27
	v_mul_f32_e32 v28, 0x43000000, v49
	v_mul_f32_e32 v27, 0x43000000, v51
	v_med3_f32 v28, v28, s35, v84
	v_med3_f32 v27, v27, s35, v84
	v_cvt_pk_fp8_f32 v26, v28, v27 op_sel:[0,0,1]
	v_mul_f32_e32 v27, 0x43000000, v53
	v_mul_f32_e32 v28, 0x43000000, v55
	v_med3_f32 v30, v27, s35, v84
	v_med3_f32 v28, v28, s35, v84
	v_mov_b32_e32 v27, v3
	v_cvt_pk_fp8_f32 v27, v30, v28
	v_mul_f32_e32 v29, 0x43000000, v57
	v_mul_f32_e32 v28, 0x43000000, v59
	v_med3_f32 v29, v29, s35, v84
	v_med3_f32 v28, v28, s35, v84
	v_cvt_pk_fp8_f32 v27, v29, v28 op_sel:[0,0,1]
	v_or_b32_e32 v28, s7, v65
	v_mul_u32_u24_e32 v28, 0x2b00, v28
	v_mov_b32_e32 v29, v3
	v_lshl_add_u64 v[60:61], v[32:33], 0, v[60:61]
	v_lshl_add_u64 v[28:29], v[32:33], 0, v[28:29]
	global_store_dwordx4 v[60:61], v[94:97], off
	global_store_dwordx4 v[28:29], v[24:27], off
	s_waitcnt lgkmcnt(0)
	s_branch .LBB0_87
.LBB0_101:
	s_andn2_b64 vcc, exec, s[0:1]
	s_cbranch_vccnz .LBB0_103
	s_add_i32 s0, s3, 0x2000
	s_and_b32 s1, s0, 0xffff
	s_mul_i32 s1, s1, 0xbe83
	s_lshr_b32 s1, s1, 24
	s_mul_i32 s7, s1, 0x158
	s_sub_i32 s0, s0, s7
	s_lshl_b32 s10, s1, 6
	v_mov_b32_e32 v24, s0
	v_pk_lshlrev_b16 v60, s52, v24 op_sel_hi:[1,0]
	v_or_b32_e32 v24, s10, v35
	v_mul_u32_u24_e32 v24, 0x2b00, v24
	v_readlane_b32 s36, v247, 41
	v_lshlrev_b32_e32 v24, 2, v24
	v_mov_b32_e32 v25, v3
	v_readlane_b32 s50, v247, 55
	v_readlane_b32 s51, v247, 56
	v_and_b32_e32 v26, 0x7fe0, v60
	v_lshlrev_b32_e32 v26, 2, v26
	v_lshl_add_u64 v[24:25], s[50:51], 0, v[24:25]
	v_mov_b32_e32 v27, v3
	v_lshl_add_u64 v[24:25], v[24:25], 0, v[26:27]
	v_lshl_add_u64 v[32:33], v[24:25], 0, v[2:3]
	v_add_co_u32_e32 v28, vcc, s53, v32
	v_mov_b32_e32 v95, v3
	s_nop 0
	v_addc_co_u32_e32 v29, vcc, 0, v33, vcc
	v_add_co_u32_e32 v36, vcc, s54, v32
	s_nop 0
	v_addc_co_u32_e32 v37, vcc, 0, v33, vcc
	v_add_co_u32_e32 v40, vcc, s55, v32
	v_mov_b32_e32 v94, v3
	s_nop 0
	v_addc_co_u32_e32 v41, vcc, 0, v33, vcc
	v_add_co_u32_e32 v44, vcc, s56, v32
	s_nop 0
	v_addc_co_u32_e32 v45, vcc, 0, v33, vcc
	v_add_co_u32_e32 v48, vcc, s57, v32
	v_mov_b32_e32 v96, v3
	s_nop 0
	v_addc_co_u32_e32 v49, vcc, 0, v33, vcc
	s_nop 0
	v_add_co_u32_e32 v52, vcc, s58, v32
	v_readfirstlane_b32 s0, v60
	s_nop 0
	v_addc_co_u32_e32 v53, vcc, 0, v33, vcc
	v_add_co_u32_e32 v32, vcc, s59, v32
	s_and_b32 s0, s0, 0x7f000060
	s_nop 0
	v_addc_co_u32_e32 v33, vcc, 0, v33, vcc
	v_mov_b32_e32 v97, v3
	s_lshr_b32 s1, s0, 16
	s_or_b32 s0, s0, s1
	s_bitset1_b32 s0, 7
	s_and_b32 s0, s0, 0xffff
	v_lshl_add_u64 v[32:33], v[6:7], 0, s[10:11]
	v_mov_b32_e32 v61, v3
	v_readlane_b32 s37, v247, 42
	v_readlane_b32 s38, v247, 43
	v_readlane_b32 s39, v247, 44
	v_readlane_b32 s40, v247, 45
	v_readlane_b32 s41, v247, 46
	v_readlane_b32 s42, v247, 47
	v_readlane_b32 s43, v247, 48
	v_readlane_b32 s44, v247, 49
	v_readlane_b32 s45, v247, 50
	v_readlane_b32 s46, v247, 51
	v_readlane_b32 s47, v247, 52
	v_readlane_b32 s48, v247, 53
	v_readlane_b32 s49, v247, 54
	s_waitcnt lgkmcnt(0)
	ds_read2_b32 v[24:25], v64 offset1:16
	ds_read2_b32 v[26:27], v64 offset0:33 offset1:49
	ds_read2_b32 v[28:29], v64 offset0:66 offset1:82
	ds_read2_b32 v[30:31], v64 offset0:99 offset1:115
	ds_read2_b32 v[36:37], v64 offset0:132 offset1:148
	ds_read2_b32 v[38:39], v64 offset0:165 offset1:181
	ds_read2_b32 v[40:41], v64 offset0:198 offset1:214
	ds_read2_b32 v[42:43], v64 offset0:231 offset1:247
	s_waitcnt lgkmcnt(7)
	v_mul_f32_e32 v24, 0x42800000, v24
	s_waitcnt lgkmcnt(3)
	v_mul_f32_e32 v36, 0x42800000, v36
	s_waitcnt lgkmcnt(2)
	v_mul_f32_e32 v38, 0x42800000, v38
	v_med3_f32 v36, v36, s35, v84
	v_med3_f32 v38, v38, s35, v84
	v_cvt_pk_fp8_f32 v95, v36, v38
	v_mul_f32_e32 v26, 0x42800000, v26
	ds_read2_b32 v[44:45], v85 offset0:8 offset1:24
	ds_read2_b32 v[46:47], v85 offset0:41 offset1:57
	ds_read2_b32 v[48:49], v85 offset0:74 offset1:90
	ds_read2_b32 v[50:51], v85 offset0:107 offset1:123
	s_waitcnt lgkmcnt(5)
	v_mul_f32_e32 v40, 0x42800000, v40
	s_waitcnt lgkmcnt(4)
	v_mul_f32_e32 v42, 0x42800000, v42
	v_med3_f32 v24, v24, s35, v84
	v_med3_f32 v26, v26, s35, v84
	v_cvt_pk_fp8_f32 v94, v24, v26
	v_med3_f32 v24, v40, s35, v84
	v_med3_f32 v26, v42, s35, v84
	v_cvt_pk_fp8_f32 v95, v24, v26 op_sel:[0,0,1]
	s_waitcnt lgkmcnt(3)
	v_mul_f32_e32 v24, 0x42800000, v44
	s_waitcnt lgkmcnt(2)
	v_mul_f32_e32 v26, 0x42800000, v46
	v_med3_f32 v24, v24, s35, v84
	v_med3_f32 v26, v26, s35, v84
	v_mul_f32_e32 v28, 0x42800000, v28
	v_mul_f32_e32 v30, 0x42800000, v30
	v_cvt_pk_fp8_f32 v96, v24, v26
	ds_read2_b32 v[52:53], v85 offset0:140 offset1:156
	ds_read2_b32 v[54:55], v85 offset0:173 offset1:189
	ds_read2_b32 v[56:57], v85 offset0:206 offset1:222
	v_med3_f32 v28, v28, s35, v84
	v_med3_f32 v30, v30, s35, v84
	v_cvt_pk_fp8_f32 v94, v28, v30 op_sel:[0,0,1]
	s_waitcnt lgkmcnt(4)
	v_mul_f32_e32 v28, 0x42800000, v48
	s_waitcnt lgkmcnt(3)
	v_mul_f32_e32 v30, 0x42800000, v50
	v_med3_f32 v24, v28, s35, v84
	v_med3_f32 v26, v30, s35, v84
	ds_read2_b32 v[58:59], v85 offset0:239 offset1:255
	v_cvt_pk_fp8_f32 v96, v24, v26 op_sel:[0,0,1]
	s_waitcnt lgkmcnt(3)
	v_mul_f32_e32 v24, 0x42800000, v52
	s_waitcnt lgkmcnt(2)
	v_mul_f32_e32 v26, 0x42800000, v54
	v_med3_f32 v24, v24, s35, v84
	v_med3_f32 v26, v26, s35, v84
	v_cvt_pk_fp8_f32 v97, v24, v26
	s_waitcnt lgkmcnt(1)
	v_mul_f32_e32 v28, 0x42800000, v56
	s_waitcnt lgkmcnt(0)
	v_mul_f32_e32 v24, 0x42800000, v58
	v_med3_f32 v26, v28, s35, v84
	v_med3_f32 v24, v24, s35, v84
	v_cvt_pk_fp8_f32 v97, v26, v24 op_sel:[0,0,1]
	v_or_b32_e32 v24, s0, v63
	v_lshlrev_b32_e32 v60, 12, v24
	v_mul_f32_e32 v24, 0x42800000, v25
	v_mul_f32_e32 v25, 0x42800000, v27
	v_med3_f32 v27, v24, s35, v84
	v_med3_f32 v25, v25, s35, v84
	v_mov_b32_e32 v24, v3
	v_cvt_pk_fp8_f32 v24, v27, v25
	v_mul_f32_e32 v26, 0x42800000, v29
	v_mul_f32_e32 v25, 0x42800000, v31
	v_med3_f32 v26, v26, s35, v84
	v_med3_f32 v25, v25, s35, v84
	v_cvt_pk_fp8_f32 v24, v26, v25 op_sel:[0,0,1]
	v_mul_f32_e32 v25, 0x42800000, v37
	v_mul_f32_e32 v26, 0x42800000, v39
	v_med3_f32 v28, v25, s35, v84
	v_med3_f32 v26, v26, s35, v84
	v_mov_b32_e32 v25, v3
	v_cvt_pk_fp8_f32 v25, v28, v26
	v_mul_f32_e32 v27, 0x42800000, v41
	v_mul_f32_e32 v26, 0x42800000, v43
	v_med3_f32 v27, v27, s35, v84
	v_med3_f32 v26, v26, s35, v84
	v_cvt_pk_fp8_f32 v25, v27, v26 op_sel:[0,0,1]
	v_mul_f32_e32 v26, 0x42800000, v45
	v_mul_f32_e32 v27, 0x42800000, v47
	v_med3_f32 v29, v26, s35, v84
	v_med3_f32 v27, v27, s35, v84
	v_mov_b32_e32 v26, v3
	v_cvt_pk_fp8_f32 v26, v29, v27
	v_mul_f32_e32 v28, 0x42800000, v49
	v_mul_f32_e32 v27, 0x42800000, v51
	v_med3_f32 v28, v28, s35, v84
	v_med3_f32 v27, v27, s35, v84
	v_cvt_pk_fp8_f32 v26, v28, v27 op_sel:[0,0,1]
	v_mul_f32_e32 v27, 0x42800000, v53
	v_mul_f32_e32 v28, 0x42800000, v55
	v_med3_f32 v30, v27, s35, v84
	v_med3_f32 v28, v28, s35, v84
	v_mov_b32_e32 v27, v3
	v_cvt_pk_fp8_f32 v27, v30, v28
	v_mul_f32_e32 v29, 0x42800000, v57
	v_mul_f32_e32 v28, 0x42800000, v59
	v_med3_f32 v29, v29, s35, v84
	v_med3_f32 v28, v28, s35, v84
	v_cvt_pk_fp8_f32 v27, v29, v28 op_sel:[0,0,1]
	v_or_b32_e32 v28, s0, v65
	v_lshlrev_b32_e32 v28, 12, v28
	v_mov_b32_e32 v29, v3
	v_lshl_add_u64 v[60:61], v[32:33], 0, v[60:61]
	v_lshl_add_u64 v[28:29], v[32:33], 0, v[28:29]
	global_store_dwordx4 v[60:61], v[94:97], off
	global_store_dwordx4 v[28:29], v[24:27], off
	s_waitcnt lgkmcnt(0)
	s_branch .LBB0_87

.LBB0_104:
	s_andn2_b64 vcc, exec, s[0:1]
	s_cbranch_vccnz .LBB0_106
	s_add_i32 s0, s3, 0x7600
	s_and_b32 s1, s0, 0xffff
	s_mul_i32 s1, s1, 0xbe83
	s_lshr_b32 s1, s1, 24
	s_mul_i32 s7, s1, 0x158
	s_sub_i32 s7, s0, s7
	s_lshl_b32 s0, s1, 6
	v_or_b32_e32 v24, s0, v35
	v_mul_u32_u24_e32 v24, 0x2b00, v24
	v_readlane_b32 s36, v247, 41
	v_lshlrev_b32_e32 v24, 2, v24
	v_mov_b32_e32 v25, v3
	v_readlane_b32 s48, v247, 53
	v_readlane_b32 s49, v247, 54
	s_lshl_b32 s1, s7, 7
	s_and_b32 s10, s1, 0x3ff80
	v_lshl_add_u64 v[24:25], s[48:49], 0, v[24:25]
	v_lshl_add_u64 v[24:25], v[24:25], 0, s[10:11]
	v_lshl_add_u64 v[32:33], v[24:25], 0, v[2:3]
	v_add_co_u32_e32 v28, vcc, s53, v32
	v_mov_b32_e32 v95, v3
	s_nop 0
	v_addc_co_u32_e32 v29, vcc, 0, v33, vcc
	v_add_co_u32_e32 v36, vcc, s54, v32
	s_nop 0
	v_addc_co_u32_e32 v37, vcc, 0, v33, vcc
	v_add_co_u32_e32 v40, vcc, s55, v32
	v_mov_b32_e32 v94, v3
	s_nop 0
	v_addc_co_u32_e32 v41, vcc, 0, v33, vcc
	v_add_co_u32_e32 v44, vcc, s56, v32
	s_nop 0
	v_addc_co_u32_e32 v45, vcc, 0, v33, vcc
	v_add_co_u32_e32 v48, vcc, s57, v32
	v_mov_b32_e32 v96, v3
	s_nop 0
	v_addc_co_u32_e32 v49, vcc, 0, v33, vcc
	s_nop 0
	v_add_co_u32_e32 v52, vcc, s58, v32
	s_mov_b32 s1, s11
	s_nop 0
	v_addc_co_u32_e32 v53, vcc, 0, v33, vcc
	v_add_co_u32_e32 v32, vcc, s59, v32
	v_mov_b32_e32 v97, v3
	s_nop 0
	v_addc_co_u32_e32 v33, vcc, 0, v33, vcc
	v_lshl_add_u64 v[32:33], v[6:7], 0, s[0:1]
	s_lshl_b32 s0, s7, 5
	s_lshl_b32 s1, s7, 6
	s_and_b32 s1, s1, 0x7f00
	s_and_b32 s0, s0, 0x60
	s_or_b32 s0, s1, s0
	s_and_b32 s0, s0, 0x7f60
	v_mov_b32_e32 v61, v3
	v_readlane_b32 s37, v247, 42
	v_readlane_b32 s38, v247, 43
	v_readlane_b32 s39, v247, 44
	v_readlane_b32 s40, v247, 45
	v_readlane_b32 s41, v247, 46
	v_readlane_b32 s42, v247, 47
	v_readlane_b32 s43, v247, 48
	v_readlane_b32 s44, v247, 49
	v_readlane_b32 s45, v247, 50
	v_readlane_b32 s46, v247, 51
	v_readlane_b32 s47, v247, 52
	v_readlane_b32 s50, v247, 55
	v_readlane_b32 s51, v247, 56
	s_waitcnt lgkmcnt(0)
	ds_read2_b32 v[24:25], v64 offset1:16
	ds_read2_b32 v[26:27], v64 offset0:33 offset1:49
	ds_read2_b32 v[28:29], v64 offset0:66 offset1:82
	ds_read2_b32 v[30:31], v64 offset0:99 offset1:115
	ds_read2_b32 v[36:37], v64 offset0:132 offset1:148
	ds_read2_b32 v[38:39], v64 offset0:165 offset1:181
	ds_read2_b32 v[40:41], v64 offset0:198 offset1:214
	ds_read2_b32 v[42:43], v64 offset0:231 offset1:247
	ds_read2_b32 v[44:45], v85 offset0:8 offset1:24
	s_waitcnt lgkmcnt(4)
	v_mul_f32_e32 v36, 0x42800000, v36
	s_waitcnt lgkmcnt(3)
	v_mul_f32_e32 v38, 0x42800000, v38
	v_med3_f32 v36, v36, s35, v84
	v_med3_f32 v38, v38, s35, v84
	v_cvt_pk_fp8_f32 v95, v36, v38
	v_mul_f32_e32 v24, 0x42800000, v24
	v_mul_f32_e32 v26, 0x42800000, v26
	ds_read2_b32 v[46:47], v85 offset0:41 offset1:57
	ds_read2_b32 v[48:49], v85 offset0:74 offset1:90
	ds_read2_b32 v[50:51], v85 offset0:107 offset1:123
	s_waitcnt lgkmcnt(5)
	v_mul_f32_e32 v40, 0x42800000, v40
	s_waitcnt lgkmcnt(4)
	v_mul_f32_e32 v42, 0x42800000, v42
	v_med3_f32 v24, v24, s35, v84
	v_med3_f32 v26, v26, s35, v84
	v_cvt_pk_fp8_f32 v94, v24, v26
	v_med3_f32 v24, v40, s35, v84
	v_med3_f32 v26, v42, s35, v84
	v_cvt_pk_fp8_f32 v95, v24, v26 op_sel:[0,0,1]
	s_waitcnt lgkmcnt(3)
	v_mul_f32_e32 v24, 0x42800000, v44
	s_waitcnt lgkmcnt(2)
	v_mul_f32_e32 v26, 0x42800000, v46
	v_med3_f32 v24, v24, s35, v84
	v_med3_f32 v26, v26, s35, v84
	v_mul_f32_e32 v28, 0x42800000, v28
	v_mul_f32_e32 v30, 0x42800000, v30
	v_cvt_pk_fp8_f32 v96, v24, v26
	ds_read2_b32 v[52:53], v85 offset0:140 offset1:156
	ds_read2_b32 v[54:55], v85 offset0:173 offset1:189
	ds_read2_b32 v[56:57], v85 offset0:206 offset1:222
	v_med3_f32 v28, v28, s35, v84
	v_med3_f32 v30, v30, s35, v84
	v_cvt_pk_fp8_f32 v94, v28, v30 op_sel:[0,0,1]
	s_waitcnt lgkmcnt(4)
	v_mul_f32_e32 v28, 0x42800000, v48
	s_waitcnt lgkmcnt(3)
	v_mul_f32_e32 v30, 0x42800000, v50
	v_med3_f32 v24, v28, s35, v84
	v_med3_f32 v26, v30, s35, v84
	ds_read2_b32 v[58:59], v85 offset0:239 offset1:255
	v_cvt_pk_fp8_f32 v96, v24, v26 op_sel:[0,0,1]
	s_waitcnt lgkmcnt(3)
	v_mul_f32_e32 v24, 0x42800000, v52
	s_waitcnt lgkmcnt(2)
	v_mul_f32_e32 v26, 0x42800000, v54
	v_med3_f32 v24, v24, s35, v84
	v_med3_f32 v26, v26, s35, v84
	v_cvt_pk_fp8_f32 v97, v24, v26
	s_waitcnt lgkmcnt(1)
	v_mul_f32_e32 v28, 0x42800000, v56
	s_waitcnt lgkmcnt(0)
	v_mul_f32_e32 v24, 0x42800000, v58
	v_med3_f32 v26, v28, s35, v84
	v_med3_f32 v24, v24, s35, v84
	v_cvt_pk_fp8_f32 v97, v26, v24 op_sel:[0,0,1]
	v_or_b32_e32 v24, s0, v63
	v_lshlrev_b32_e32 v60, 12, v24
	v_mul_f32_e32 v24, 0x42800000, v25
	v_mul_f32_e32 v25, 0x42800000, v27
	v_med3_f32 v27, v24, s35, v84
	v_med3_f32 v25, v25, s35, v84
	v_mov_b32_e32 v24, v3
	v_cvt_pk_fp8_f32 v24, v27, v25
	v_mul_f32_e32 v26, 0x42800000, v29
	v_mul_f32_e32 v25, 0x42800000, v31
	v_med3_f32 v26, v26, s35, v84
	v_med3_f32 v25, v25, s35, v84
	v_cvt_pk_fp8_f32 v24, v26, v25 op_sel:[0,0,1]
	v_mul_f32_e32 v25, 0x42800000, v37
	v_mul_f32_e32 v26, 0x42800000, v39
	v_med3_f32 v28, v25, s35, v84
	v_med3_f32 v26, v26, s35, v84
	v_mov_b32_e32 v25, v3
	v_cvt_pk_fp8_f32 v25, v28, v26
	v_mul_f32_e32 v27, 0x42800000, v41
	v_mul_f32_e32 v26, 0x42800000, v43
	v_med3_f32 v27, v27, s35, v84
	v_med3_f32 v26, v26, s35, v84
	v_cvt_pk_fp8_f32 v25, v27, v26 op_sel:[0,0,1]
	v_mul_f32_e32 v26, 0x42800000, v45
	v_mul_f32_e32 v27, 0x42800000, v47
	v_med3_f32 v29, v26, s35, v84
	v_med3_f32 v27, v27, s35, v84
	v_mov_b32_e32 v26, v3
	v_cvt_pk_fp8_f32 v26, v29, v27
	v_mul_f32_e32 v28, 0x42800000, v49
	v_mul_f32_e32 v27, 0x42800000, v51
	v_med3_f32 v28, v28, s35, v84
	v_med3_f32 v27, v27, s35, v84
	v_cvt_pk_fp8_f32 v26, v28, v27 op_sel:[0,0,1]
	v_mul_f32_e32 v27, 0x42800000, v53
	v_mul_f32_e32 v28, 0x42800000, v55
	v_med3_f32 v30, v27, s35, v84
	v_med3_f32 v28, v28, s35, v84
	v_mov_b32_e32 v27, v3
	v_cvt_pk_fp8_f32 v27, v30, v28
	v_mul_f32_e32 v29, 0x42800000, v57
	v_mul_f32_e32 v28, 0x42800000, v59
	v_med3_f32 v29, v29, s35, v84
	v_med3_f32 v28, v28, s35, v84
	v_cvt_pk_fp8_f32 v27, v29, v28 op_sel:[0,0,1]
	v_or_b32_e32 v28, s0, v65
	v_lshlrev_b32_e32 v28, 12, v28
	v_mov_b32_e32 v29, v3
	v_lshl_add_u64 v[60:61], v[32:33], 0, v[60:61]
	v_lshl_add_u64 v[28:29], v[32:33], 0, v[28:29]
	global_store_dwordx4 v[60:61], v[94:97], off
	global_store_dwordx4 v[28:29], v[24:27], off
	s_waitcnt lgkmcnt(0)
	s_branch .LBB0_87

.LBB0_107:
	s_andn2_b64 vcc, exec, s[0:1]
	s_cbranch_vccnz .LBB0_109
	s_add_i32 s0, s3, 0x7a00
	s_lshr_b32 s0, s0, 1
	s_and_b32 s0, s0, 0x7fc0
	s_lshl_b32 s1, s3, 5
	v_or_b32_e32 v24, s0, v35
	v_readlane_b32 s36, v247, 41
	s_and_b32 s7, s1, 0xfe0
	v_lshlrev_b32_e32 v24, 14, v24
	v_mov_b32_e32 v25, v3
	v_readlane_b32 s44, v247, 49
	v_readlane_b32 s45, v247, 50
	s_lshl_b32 s10, s7, 2
	v_mov_b32_e32 v94, v3
	v_lshl_add_u64 v[24:25], s[44:45], 0, v[24:25]
	v_lshl_add_u64 v[24:25], v[24:25], 0, s[10:11]
	v_lshl_add_u64 v[32:33], v[24:25], 0, v[2:3]
	v_add_co_u32_e32 v28, vcc, s18, v32
	v_mov_b32_e32 v95, v3
	s_nop 0
	v_addc_co_u32_e32 v29, vcc, 0, v33, vcc
	v_add_co_u32_e32 v36, vcc, s19, v32
	s_nop 0
	v_addc_co_u32_e32 v37, vcc, 0, v33, vcc
	v_add_co_u32_e32 v40, vcc, s20, v32
	v_mov_b32_e32 v96, v3
	s_nop 0
	v_addc_co_u32_e32 v41, vcc, 0, v33, vcc
	v_add_co_u32_e32 v44, vcc, s21, v32
	s_nop 0
	v_addc_co_u32_e32 v45, vcc, 0, v33, vcc
	v_add_co_u32_e32 v48, vcc, s30, v32
	v_mov_b32_e32 v97, v3
	s_nop 0
	v_addc_co_u32_e32 v49, vcc, 0, v33, vcc
	s_nop 0
	v_add_co_u32_e32 v52, vcc, s31, v32
	s_mov_b32 s1, s11
	s_nop 0
	v_addc_co_u32_e32 v53, vcc, 0, v33, vcc
	v_add_co_u32_e32 v32, vcc, s34, v32
	v_mov_b32_e32 v61, v3
	s_nop 0
	v_addc_co_u32_e32 v33, vcc, 0, v33, vcc
	v_lshl_add_u64 v[32:33], v[8:9], 0, s[0:1]
	v_readlane_b32 s37, v247, 42
	v_readlane_b32 s38, v247, 43
	v_readlane_b32 s39, v247, 44
	v_readlane_b32 s40, v247, 45
	v_readlane_b32 s41, v247, 46
	v_readlane_b32 s42, v247, 47
	v_readlane_b32 s43, v247, 48
	v_readlane_b32 s46, v247, 51
	v_readlane_b32 s47, v247, 52
	v_readlane_b32 s48, v247, 53
	v_readlane_b32 s49, v247, 54
	v_readlane_b32 s50, v247, 55
	v_readlane_b32 s51, v247, 56
	s_waitcnt lgkmcnt(0)
	ds_read2_b32 v[24:25], v64 offset1:16
	ds_read2_b32 v[26:27], v64 offset0:33 offset1:49
	ds_read2_b32 v[28:29], v64 offset0:66 offset1:82
	ds_read2_b32 v[30:31], v64 offset0:99 offset1:115
	ds_read2_b32 v[36:37], v64 offset0:132 offset1:148
	ds_read2_b32 v[38:39], v64 offset0:165 offset1:181
	ds_read2_b32 v[40:41], v64 offset0:198 offset1:214
	ds_read2_b32 v[42:43], v64 offset0:231 offset1:247
	ds_read2_b32 v[44:45], v85 offset0:8 offset1:24
	ds_read2_b32 v[46:47], v85 offset0:41 offset1:57
	ds_read2_b32 v[48:49], v85 offset0:74 offset1:90
	ds_read2_b32 v[50:51], v85 offset0:107 offset1:123
	s_waitcnt lgkmcnt(11)
	v_mul_f32_e32 v24, 0x42800000, v24
	s_waitcnt lgkmcnt(10)
	v_mul_f32_e32 v26, 0x42800000, v26
	s_waitcnt lgkmcnt(7)
	v_mul_f32_e32 v36, 0x42800000, v36
	s_waitcnt lgkmcnt(6)
	v_mul_f32_e32 v38, 0x42800000, v38
	v_med3_f32 v24, v24, s35, v84
	v_med3_f32 v26, v26, s35, v84
	v_med3_f32 v36, v36, s35, v84
	v_med3_f32 v38, v38, s35, v84
	v_cvt_pk_fp8_f32 v94, v24, v26
	v_cvt_pk_fp8_f32 v95, v36, v38
	v_mul_f32_e32 v28, 0x42800000, v28
	v_mul_f32_e32 v30, 0x42800000, v30
	s_waitcnt lgkmcnt(5)
	v_mul_f32_e32 v40, 0x42800000, v40
	s_waitcnt lgkmcnt(4)
	v_mul_f32_e32 v42, 0x42800000, v42
	s_waitcnt lgkmcnt(3)
	v_mul_f32_e32 v44, 0x42800000, v44
	s_waitcnt lgkmcnt(2)
	v_mul_f32_e32 v46, 0x42800000, v46
	v_med3_f32 v28, v28, s35, v84
	v_med3_f32 v30, v30, s35, v84
	v_med3_f32 v24, v40, s35, v84
	v_med3_f32 v26, v42, s35, v84
	v_cvt_pk_fp8_f32 v94, v28, v30 op_sel:[0,0,1]
	v_cvt_pk_fp8_f32 v95, v24, v26 op_sel:[0,0,1]
	v_med3_f32 v26, v44, s35, v84
	v_med3_f32 v28, v46, s35, v84
	v_cvt_pk_fp8_f32 v96, v26, v28
	ds_read2_b32 v[52:53], v85 offset0:140 offset1:156
	ds_read2_b32 v[54:55], v85 offset0:173 offset1:189
	ds_read2_b32 v[56:57], v85 offset0:206 offset1:222
	s_waitcnt lgkmcnt(4)
	v_mul_f32_e32 v48, 0x42800000, v48
	s_waitcnt lgkmcnt(3)
	v_mul_f32_e32 v24, 0x42800000, v50
	v_med3_f32 v26, v48, s35, v84
	v_med3_f32 v24, v24, s35, v84
	ds_read2_b32 v[58:59], v85 offset0:239 offset1:255
	v_cvt_pk_fp8_f32 v96, v26, v24 op_sel:[0,0,1]
	s_waitcnt lgkmcnt(3)
	v_mul_f32_e32 v24, 0x42800000, v52
	s_waitcnt lgkmcnt(2)
	v_mul_f32_e32 v26, 0x42800000, v54
	v_med3_f32 v24, v24, s35, v84
	v_med3_f32 v26, v26, s35, v84
	v_cvt_pk_fp8_f32 v97, v24, v26
	s_waitcnt lgkmcnt(1)
	v_mul_f32_e32 v28, 0x42800000, v56
	s_waitcnt lgkmcnt(0)
	v_mul_f32_e32 v24, 0x42800000, v58
	v_med3_f32 v26, v28, s35, v84
	v_med3_f32 v24, v24, s35, v84
	v_cvt_pk_fp8_f32 v97, v26, v24 op_sel:[0,0,1]
	v_or_b32_e32 v24, s7, v63
	v_lshlrev_b32_e32 v60, 9, v24
	v_mul_f32_e32 v24, 0x42800000, v25
	v_mul_f32_e32 v25, 0x42800000, v27
	v_med3_f32 v27, v24, s35, v84
	v_med3_f32 v25, v25, s35, v84
	v_mov_b32_e32 v24, v3
	v_cvt_pk_fp8_f32 v24, v27, v25
	v_mul_f32_e32 v26, 0x42800000, v29
	v_mul_f32_e32 v25, 0x42800000, v31
	v_med3_f32 v26, v26, s35, v84
	v_med3_f32 v25, v25, s35, v84
	v_cvt_pk_fp8_f32 v24, v26, v25 op_sel:[0,0,1]
	v_mul_f32_e32 v25, 0x42800000, v37
	v_mul_f32_e32 v26, 0x42800000, v39
	v_med3_f32 v28, v25, s35, v84
	v_med3_f32 v26, v26, s35, v84
	v_mov_b32_e32 v25, v3
	v_cvt_pk_fp8_f32 v25, v28, v26
	v_mul_f32_e32 v27, 0x42800000, v41
	v_mul_f32_e32 v26, 0x42800000, v43
	v_med3_f32 v27, v27, s35, v84
	v_med3_f32 v26, v26, s35, v84
	v_cvt_pk_fp8_f32 v25, v27, v26 op_sel:[0,0,1]
	v_mul_f32_e32 v26, 0x42800000, v45
	v_mul_f32_e32 v27, 0x42800000, v47
	v_med3_f32 v29, v26, s35, v84
	v_med3_f32 v27, v27, s35, v84
	v_mov_b32_e32 v26, v3
	v_cvt_pk_fp8_f32 v26, v29, v27
	v_mul_f32_e32 v28, 0x42800000, v49
	v_mul_f32_e32 v27, 0x42800000, v51
	v_med3_f32 v28, v28, s35, v84
	v_med3_f32 v27, v27, s35, v84
	v_cvt_pk_fp8_f32 v26, v28, v27 op_sel:[0,0,1]
	v_mul_f32_e32 v27, 0x42800000, v53
	v_mul_f32_e32 v28, 0x42800000, v55
	v_med3_f32 v30, v27, s35, v84
	v_med3_f32 v28, v28, s35, v84
	v_mov_b32_e32 v27, v3
	v_cvt_pk_fp8_f32 v27, v30, v28
	v_mul_f32_e32 v29, 0x42800000, v57
	v_mul_f32_e32 v28, 0x42800000, v59
	v_med3_f32 v29, v29, s35, v84
	v_med3_f32 v28, v28, s35, v84
	v_cvt_pk_fp8_f32 v27, v29, v28 op_sel:[0,0,1]
	v_or_b32_e32 v28, s7, v65
	v_lshlrev_b32_e32 v28, 9, v28
	v_mov_b32_e32 v29, v3
	v_lshl_add_u64 v[60:61], v[32:33], 0, v[60:61]
	v_lshl_add_u64 v[28:29], v[32:33], 0, v[28:29]
	global_store_dwordx4 v[60:61], v[94:97], off
	global_store_dwordx4 v[28:29], v[24:27], off
	s_waitcnt lgkmcnt(0)
	s_branch .LBB0_87

.LBB0_110:
	s_andn2_b64 vcc, exec, s[0:1]
	s_cbranch_vccnz .LBB0_112
	s_and_b32 s1, s16, 0x3ffc0
	s_lshl_b32 s0, s3, 5
	v_or_b32_e32 v24, s1, v35
	v_readlane_b32 s36, v247, 41
	s_and_b32 s7, s0, 0x1e0
	v_lshlrev_b32_e32 v24, 11, v24
	v_mov_b32_e32 v25, v3
	v_readlane_b32 s42, v247, 47
	v_readlane_b32 s43, v247, 48
	s_lshl_b32 s10, s7, 2
	s_bitset1_b32 s0, 9
	v_lshl_add_u64 v[24:25], s[42:43], 0, v[24:25]
	v_lshl_add_u64 v[24:25], v[24:25], 0, s[10:11]
	v_lshl_add_u64 v[32:33], v[24:25], 0, v[2:3]
	v_add_co_u32_e32 v28, vcc, s72, v32
	s_and_b32 s0, s0, 0x3e0
	s_nop 0
	v_addc_co_u32_e32 v29, vcc, 0, v33, vcc
	v_add_co_u32_e32 v36, vcc, s73, v32
	s_nop 0
	v_addc_co_u32_e32 v37, vcc, 0, v33, vcc
	v_add_co_u32_e32 v40, vcc, s74, v32
	s_lshl_b32 s10, s1, 1
	s_nop 0
	v_addc_co_u32_e32 v41, vcc, 0, v33, vcc
	v_add_co_u32_e32 v44, vcc, s75, v32
	s_nop 0
	v_addc_co_u32_e32 v45, vcc, 0, v33, vcc
	v_add_co_u32_e32 v48, vcc, s64, v32
	v_readlane_b32 s37, v247, 42
	s_nop 0
	v_addc_co_u32_e32 v49, vcc, 0, v33, vcc
	s_nop 0
	v_add_co_u32_e32 v52, vcc, s65, v32
	v_readlane_b32 s38, v247, 43
	s_nop 0
	v_addc_co_u32_e32 v53, vcc, 0, v33, vcc
	v_add_co_u32_e32 v32, vcc, s66, v32
	v_readlane_b32 s39, v247, 44
	s_nop 0
	v_addc_co_u32_e32 v33, vcc, 0, v33, vcc
	v_lshl_add_u64 v[32:33], v[10:11], 0, s[10:11]
	v_readlane_b32 s40, v247, 45
	v_readlane_b32 s41, v247, 46
	v_readlane_b32 s44, v247, 49
	v_readlane_b32 s45, v247, 50
	v_readlane_b32 s46, v247, 51
	v_readlane_b32 s47, v247, 52
	v_readlane_b32 s48, v247, 53
	v_readlane_b32 s49, v247, 54
	v_readlane_b32 s50, v247, 55
	v_readlane_b32 s51, v247, 56
	s_waitcnt lgkmcnt(0)
	ds_read2_b32 v[28:29], v66 offset0:33 offset1:41
	ds_read2_b32 v[30:31], v66 offset1:8
	ds_read2_b32 v[36:37], v66 offset0:66 offset1:74
	ds_read2_b32 v[38:39], v66 offset0:99 offset1:107
	ds_read2_b32 v[40:41], v66 offset0:132 offset1:140
	ds_read2_b32 v[42:43], v66 offset0:165 offset1:173
	ds_read2_b32 v[44:45], v66 offset0:198 offset1:206
	ds_read2_b32 v[46:47], v66 offset0:231 offset1:239
	s_waitcnt lgkmcnt(6)
	v_bfe_u32 v24, v30, 16, 1
	v_bfe_u32 v25, v28, 16, 1
	s_waitcnt lgkmcnt(5)
	v_bfe_u32 v26, v36, 16, 1
	s_waitcnt lgkmcnt(3)
	v_bfe_u32 v48, v40, 16, 1
	v_bfe_u32 v27, v38, 16, 1
	s_waitcnt lgkmcnt(2)
	v_bfe_u32 v49, v42, 16, 1
	v_add3_u32 v24, v30, v24, s67
	v_add3_u32 v25, v28, v25, s67
	v_add3_u32 v26, v36, v26, s67
	v_add3_u32 v28, v40, v48, s67
	s_waitcnt lgkmcnt(1)
	v_bfe_u32 v50, v44, 16, 1
	v_add3_u32 v27, v38, v27, s67
	v_add3_u32 v30, v42, v49, s67
	v_lshrrev_b32_e32 v24, 16, v24
	v_lshrrev_b32_e32 v26, 16, v26
	v_lshrrev_b32_e32 v28, 16, v28
	s_waitcnt lgkmcnt(0)
	v_bfe_u32 v51, v46, 16, 1
	v_add3_u32 v36, v44, v50, s67
	v_and_or_b32 v24, v25, s68, v24
	v_and_or_b32 v25, v27, s68, v26
	v_and_or_b32 v26, v30, s68, v28
	v_or_b32_e32 v28, s0, v35
	v_add3_u32 v38, v46, v51, s67
	v_lshrrev_b32_e32 v36, 16, v36
	v_lshlrev_b32_e32 v48, 13, v28
	v_mov_b32_e32 v49, v3
	v_and_or_b32 v27, v38, s68, v36
	v_lshl_add_u64 v[48:49], v[32:33], 0, v[48:49]
	global_store_dwordx4 v[48:49], v[24:27], off
	v_bfe_u32 v28, v47, 16, 1
	v_add3_u32 v28, v47, v28, s67
	v_bfe_u32 v24, v31, 16, 1
	v_add3_u32 v24, v31, v24, s67
	v_bfe_u32 v25, v29, 16, 1
	v_lshrrev_b32_e32 v24, 16, v24
	v_add3_u32 v25, v29, v25, s67
	v_and_or_b32 v24, v25, s68, v24
	v_bfe_u32 v25, v37, 16, 1
	v_add3_u32 v25, v37, v25, s67
	v_bfe_u32 v26, v39, 16, 1
	v_lshrrev_b32_e32 v25, 16, v25
	v_add3_u32 v26, v39, v26, s67
	v_and_or_b32 v25, v26, s68, v25
	v_bfe_u32 v26, v41, 16, 1
	v_add3_u32 v26, v41, v26, s67
	v_bfe_u32 v27, v43, 16, 1
	v_lshrrev_b32_e32 v26, 16, v26
	v_add3_u32 v27, v43, v27, s67
	v_and_or_b32 v26, v27, s68, v26
	v_bfe_u32 v27, v45, 16, 1
	v_add3_u32 v27, v45, v27, s67
	v_lshrrev_b32_e32 v27, 16, v27
	v_and_or_b32 v27, v28, s68, v27
	v_or_b32_e32 v28, s0, v67
	v_lshlrev_b32_e32 v28, 13, v28
	v_mov_b32_e32 v29, v3
	ds_read2_b32 v[30:31], v66 offset0:16 offset1:24
	v_lshl_add_u64 v[28:29], v[32:33], 0, v[28:29]
	global_store_dwordx4 v[28:29], v[24:27], off
	ds_read2_b32 v[28:29], v66 offset0:49 offset1:57
	ds_read2_b32 v[36:37], v66 offset0:82 offset1:90
	ds_read2_b32 v[38:39], v66 offset0:115 offset1:123
	s_waitcnt lgkmcnt(3)
	v_bfe_u32 v24, v30, 16, 1
	v_add3_u32 v24, v30, v24, s67
	s_waitcnt lgkmcnt(2)
	v_bfe_u32 v25, v28, 16, 1
	ds_read2_b32 v[40:41], v66 offset0:148 offset1:156
	v_lshrrev_b32_e32 v24, 16, v24
	v_add3_u32 v25, v28, v25, s67
	ds_read2_b32 v[42:43], v66 offset0:181 offset1:189
	v_and_or_b32 v24, v25, s68, v24
	s_waitcnt lgkmcnt(3)
	v_bfe_u32 v25, v36, 16, 1
	v_add3_u32 v25, v36, v25, s67
	s_waitcnt lgkmcnt(2)
	v_bfe_u32 v26, v38, 16, 1
	ds_read2_b32 v[44:45], v66 offset0:214 offset1:222
	v_lshrrev_b32_e32 v25, 16, v25
	v_add3_u32 v26, v38, v26, s67
	ds_read2_b32 v[46:47], v66 offset0:247 offset1:255
	v_and_or_b32 v25, v26, s68, v25
	s_waitcnt lgkmcnt(3)
	v_bfe_u32 v26, v40, 16, 1
	v_add3_u32 v26, v40, v26, s67
	s_waitcnt lgkmcnt(2)
	v_bfe_u32 v27, v42, 16, 1
	v_lshrrev_b32_e32 v26, 16, v26
	v_add3_u32 v27, v42, v27, s67
	v_and_or_b32 v26, v27, s68, v26
	s_waitcnt lgkmcnt(1)
	v_bfe_u32 v27, v44, 16, 1
	v_add3_u32 v27, v44, v27, s67
	s_waitcnt lgkmcnt(0)
	v_bfe_u32 v28, v46, 16, 1
	v_lshrrev_b32_e32 v27, 16, v27
	v_add3_u32 v28, v46, v28, s67
	v_and_or_b32 v27, v28, s68, v27
	v_or_b32_e32 v28, s0, v68
	v_lshlrev_b32_e32 v48, 13, v28
	v_mov_b32_e32 v49, v3
	v_lshl_add_u64 v[48:49], v[32:33], 0, v[48:49]
	global_store_dwordx4 v[48:49], v[24:27], off
	v_bfe_u32 v28, v47, 16, 1
	v_add3_u32 v28, v47, v28, s67
	v_bfe_u32 v24, v31, 16, 1
	v_add3_u32 v24, v31, v24, s67
	v_bfe_u32 v25, v29, 16, 1
	v_lshrrev_b32_e32 v24, 16, v24
	v_add3_u32 v25, v29, v25, s67
	v_and_or_b32 v24, v25, s68, v24
	v_bfe_u32 v25, v37, 16, 1
	v_add3_u32 v25, v37, v25, s67
	v_bfe_u32 v26, v39, 16, 1
	v_lshrrev_b32_e32 v25, 16, v25
	v_add3_u32 v26, v39, v26, s67
	v_and_or_b32 v25, v26, s68, v25
	v_bfe_u32 v26, v41, 16, 1
	v_add3_u32 v26, v41, v26, s67
	v_bfe_u32 v27, v43, 16, 1
	v_lshrrev_b32_e32 v26, 16, v26
	v_add3_u32 v27, v43, v27, s67
	v_and_or_b32 v26, v27, s68, v26
	v_bfe_u32 v27, v45, 16, 1
	v_add3_u32 v27, v45, v27, s67
	v_lshrrev_b32_e32 v27, 16, v27
	v_and_or_b32 v27, v28, s68, v27
	v_or_b32_e32 v28, s0, v69
	v_lshlrev_b32_e32 v28, 13, v28
	v_mov_b32_e32 v29, v3
	v_lshl_add_u64 v[28:29], v[32:33], 0, v[28:29]
	global_store_dwordx4 v[28:29], v[24:27], off
	s_waitcnt lgkmcnt(0)
	s_branch .LBB0_87

.LBB0_113:
	s_andn2_b64 vcc, exec, s[0:1]
	s_cbranch_vccnz .LBB0_115
	s_add_i32 s0, s16, 0x1000
	s_and_b32 s1, s0, 0x3ffc0
	s_lshl_b32 s0, s3, 5
	v_or_b32_e32 v24, s1, v35
	v_readlane_b32 s36, v247, 41
	s_and_b32 s0, s0, 0x1e0
	v_lshlrev_b32_e32 v24, 11, v24
	v_mov_b32_e32 v25, v3
	v_readlane_b32 s40, v247, 45
	v_readlane_b32 s41, v247, 46
	s_lshl_b32 s10, s0, 2
	v_readlane_b32 s37, v247, 42
	v_lshl_add_u64 v[24:25], s[40:41], 0, v[24:25]
	v_lshl_add_u64 v[24:25], v[24:25], 0, s[10:11]
	v_lshl_add_u64 v[32:33], v[24:25], 0, v[2:3]
	v_add_co_u32_e32 v28, vcc, s72, v32
	s_lshl_b32 s10, s1, 1
	s_nop 0
	v_addc_co_u32_e32 v29, vcc, 0, v33, vcc
	v_add_co_u32_e32 v36, vcc, s73, v32
	s_nop 0
	v_addc_co_u32_e32 v37, vcc, 0, v33, vcc
	v_add_co_u32_e32 v40, vcc, s74, v32
	v_lshl_add_u64 v[60:61], v[10:11], 0, s[10:11]
	s_nop 0
	v_addc_co_u32_e32 v41, vcc, 0, v33, vcc
	v_add_co_u32_e32 v44, vcc, s75, v32
	s_nop 0
	v_addc_co_u32_e32 v45, vcc, 0, v33, vcc
	v_add_co_u32_e32 v48, vcc, s64, v32
	v_readlane_b32 s38, v247, 43
	s_nop 0
	v_addc_co_u32_e32 v49, vcc, 0, v33, vcc
	s_nop 0
	v_add_co_u32_e32 v52, vcc, s65, v32
	v_readlane_b32 s39, v247, 44
	s_nop 0
	v_addc_co_u32_e32 v53, vcc, 0, v33, vcc
	v_add_co_u32_e32 v32, vcc, s66, v32
	v_readlane_b32 s42, v247, 47
	s_nop 0
	v_addc_co_u32_e32 v33, vcc, 0, v33, vcc
	v_or_b32_e32 v32, s0, v35
	v_lshlrev_b32_e32 v32, 13, v32
	v_readlane_b32 s43, v247, 48
	v_readlane_b32 s44, v247, 49
	v_readlane_b32 s45, v247, 50
	v_readlane_b32 s46, v247, 51
	v_readlane_b32 s47, v247, 52
	v_readlane_b32 s48, v247, 53
	v_readlane_b32 s49, v247, 54
	v_readlane_b32 s50, v247, 55
	v_readlane_b32 s51, v247, 56
	s_waitcnt lgkmcnt(0)
	ds_read2_b32 v[28:29], v66 offset0:33 offset1:41
	ds_read2_b32 v[30:31], v66 offset1:8
	ds_read2_b32 v[36:37], v66 offset0:66 offset1:74
	ds_read2_b32 v[38:39], v66 offset0:99 offset1:107
	ds_read2_b32 v[40:41], v66 offset0:132 offset1:140
	ds_read2_b32 v[42:43], v66 offset0:165 offset1:173
	ds_read2_b32 v[44:45], v66 offset0:198 offset1:206
	ds_read2_b32 v[46:47], v66 offset0:231 offset1:239
	s_waitcnt lgkmcnt(6)
	v_bfe_u32 v24, v30, 16, 1
	v_bfe_u32 v25, v28, 16, 1
	s_waitcnt lgkmcnt(5)
	v_bfe_u32 v26, v36, 16, 1
	s_waitcnt lgkmcnt(3)
	v_bfe_u32 v33, v40, 16, 1
	s_waitcnt lgkmcnt(1)
	v_bfe_u32 v49, v44, 16, 1
	v_bfe_u32 v27, v38, 16, 1
	s_waitcnt lgkmcnt(0)
	v_bfe_u32 v50, v46, 16, 1
	v_add3_u32 v24, v30, v24, s67
	v_add3_u32 v25, v28, v25, s67
	v_add3_u32 v26, v36, v26, s67
	v_add3_u32 v28, v40, v33, s67
	v_add3_u32 v33, v44, v49, s67
	v_bfe_u32 v48, v42, 16, 1
	v_add3_u32 v27, v38, v27, s67
	v_add3_u32 v36, v46, v50, s67
	v_lshrrev_b32_e32 v24, 16, v24
	v_lshrrev_b32_e32 v26, 16, v26
	v_lshrrev_b32_e32 v33, 16, v33
	v_add3_u32 v30, v42, v48, s67
	v_lshrrev_b32_e32 v28, 16, v28
	v_and_or_b32 v24, v25, s68, v24
	v_and_or_b32 v25, v27, s68, v26
	v_and_or_b32 v27, v36, s68, v33
	v_mov_b32_e32 v33, v3
	v_and_or_b32 v26, v30, s68, v28
	v_lshl_add_u64 v[32:33], v[60:61], 0, v[32:33]
	global_store_dwordx4 v[32:33], v[24:27], off
	v_bfe_u32 v28, v47, 16, 1
	v_add3_u32 v28, v47, v28, s67
	v_bfe_u32 v24, v31, 16, 1
	v_add3_u32 v24, v31, v24, s67
	v_bfe_u32 v25, v29, 16, 1
	v_lshrrev_b32_e32 v24, 16, v24
	v_add3_u32 v25, v29, v25, s67
	v_and_or_b32 v24, v25, s68, v24
	v_bfe_u32 v25, v37, 16, 1
	v_add3_u32 v25, v37, v25, s67
	v_bfe_u32 v26, v39, 16, 1
	v_lshrrev_b32_e32 v25, 16, v25
	v_add3_u32 v26, v39, v26, s67
	v_and_or_b32 v25, v26, s68, v25
	v_bfe_u32 v26, v41, 16, 1
	v_add3_u32 v26, v41, v26, s67
	v_bfe_u32 v27, v43, 16, 1
	v_lshrrev_b32_e32 v26, 16, v26
	v_add3_u32 v27, v43, v27, s67
	v_and_or_b32 v26, v27, s68, v26
	v_bfe_u32 v27, v45, 16, 1
	v_add3_u32 v27, v45, v27, s67
	v_lshrrev_b32_e32 v27, 16, v27
	v_and_or_b32 v27, v28, s68, v27
	v_or_b32_e32 v28, s0, v67
	v_lshlrev_b32_e32 v28, 13, v28
	v_mov_b32_e32 v29, v3
	ds_read2_b32 v[30:31], v66 offset0:16 offset1:24
	v_lshl_add_u64 v[28:29], v[60:61], 0, v[28:29]
	global_store_dwordx4 v[28:29], v[24:27], off
	ds_read2_b32 v[28:29], v66 offset0:49 offset1:57
	ds_read2_b32 v[32:33], v66 offset0:82 offset1:90
	ds_read2_b32 v[36:37], v66 offset0:115 offset1:123
	s_waitcnt lgkmcnt(3)
	v_bfe_u32 v24, v30, 16, 1
	v_add3_u32 v24, v30, v24, s67
	s_waitcnt lgkmcnt(2)
	v_bfe_u32 v25, v28, 16, 1
	ds_read2_b32 v[38:39], v66 offset0:148 offset1:156
	v_lshrrev_b32_e32 v24, 16, v24
	v_add3_u32 v25, v28, v25, s67
	ds_read2_b32 v[40:41], v66 offset0:181 offset1:189
	v_and_or_b32 v24, v25, s68, v24
	s_waitcnt lgkmcnt(3)
	v_bfe_u32 v25, v32, 16, 1
	v_add3_u32 v25, v32, v25, s67
	s_waitcnt lgkmcnt(2)
	v_bfe_u32 v26, v36, 16, 1
	ds_read2_b32 v[42:43], v66 offset0:214 offset1:222
	v_lshrrev_b32_e32 v25, 16, v25
	v_add3_u32 v26, v36, v26, s67
	ds_read2_b32 v[44:45], v66 offset0:247 offset1:255
	v_and_or_b32 v25, v26, s68, v25
	s_waitcnt lgkmcnt(3)
	v_bfe_u32 v26, v38, 16, 1
	v_add3_u32 v26, v38, v26, s67
	s_waitcnt lgkmcnt(2)
	v_bfe_u32 v27, v40, 16, 1
	v_lshrrev_b32_e32 v26, 16, v26
	v_add3_u32 v27, v40, v27, s67
	v_and_or_b32 v26, v27, s68, v26
	s_waitcnt lgkmcnt(1)
	v_bfe_u32 v27, v42, 16, 1
	v_add3_u32 v27, v42, v27, s67
	s_waitcnt lgkmcnt(0)
	v_bfe_u32 v28, v44, 16, 1
	v_lshrrev_b32_e32 v27, 16, v27
	v_add3_u32 v28, v44, v28, s67
	v_and_or_b32 v27, v28, s68, v27
	v_or_b32_e32 v28, s0, v68
	v_lshlrev_b32_e32 v46, 13, v28
	v_mov_b32_e32 v47, v3
	v_lshl_add_u64 v[46:47], v[60:61], 0, v[46:47]
	global_store_dwordx4 v[46:47], v[24:27], off
	v_bfe_u32 v28, v45, 16, 1
	v_add3_u32 v28, v45, v28, s67
	v_bfe_u32 v24, v31, 16, 1
	v_add3_u32 v24, v31, v24, s67
	v_bfe_u32 v25, v29, 16, 1
	v_lshrrev_b32_e32 v24, 16, v24
	v_add3_u32 v25, v29, v25, s67
	v_and_or_b32 v24, v25, s68, v24
	v_bfe_u32 v25, v33, 16, 1
	v_add3_u32 v25, v33, v25, s67
	v_bfe_u32 v26, v37, 16, 1
	v_lshrrev_b32_e32 v25, 16, v25
	v_add3_u32 v26, v37, v26, s67
	v_and_or_b32 v25, v26, s68, v25
	v_bfe_u32 v26, v39, 16, 1
	v_add3_u32 v26, v39, v26, s67
	v_bfe_u32 v27, v41, 16, 1
	v_lshrrev_b32_e32 v26, 16, v26
	v_add3_u32 v27, v41, v27, s67
	v_and_or_b32 v26, v27, s68, v26
	v_bfe_u32 v27, v43, 16, 1
	v_add3_u32 v27, v43, v27, s67
	v_lshrrev_b32_e32 v27, 16, v27
	v_and_or_b32 v27, v28, s68, v27
	v_or_b32_e32 v28, s0, v69
	v_lshlrev_b32_e32 v28, 13, v28
	v_mov_b32_e32 v29, v3
	v_lshl_add_u64 v[28:29], v[60:61], 0, v[28:29]
	global_store_dwordx4 v[28:29], v[24:27], off
	s_waitcnt lgkmcnt(0)
	s_branch .LBB0_87

.LBB0_116:
	s_andn2_b64 vcc, exec, s[0:1]
	s_cbranch_vccnz .LBB0_118
	s_add_i32 s0, s16, 0x2000
	s_and_b32 s0, s0, 0x3ffc0
	s_lshl_b32 s1, s3, 5
	v_or_b32_e32 v24, s0, v35
	v_readlane_b32 s36, v247, 41
	s_and_b32 s7, s1, 0x1e0
	v_lshlrev_b32_e32 v24, 11, v24
	v_mov_b32_e32 v25, v3
	v_readlane_b32 s38, v247, 43
	v_readlane_b32 s39, v247, 44
	s_lshl_b32 s10, s7, 2
	v_mov_b32_e32 v94, v3
	v_lshl_add_u64 v[24:25], s[38:39], 0, v[24:25]
	v_lshl_add_u64 v[24:25], v[24:25], 0, s[10:11]
	v_lshl_add_u64 v[32:33], v[24:25], 0, v[2:3]
	v_add_co_u32_e32 v28, vcc, s72, v32
	v_mov_b32_e32 v95, v3
	s_nop 0
	v_addc_co_u32_e32 v29, vcc, 0, v33, vcc
	v_add_co_u32_e32 v36, vcc, s73, v32
	s_nop 0
	v_addc_co_u32_e32 v37, vcc, 0, v33, vcc
	v_add_co_u32_e32 v40, vcc, s74, v32
	v_mov_b32_e32 v96, v3
	s_nop 0
	v_addc_co_u32_e32 v41, vcc, 0, v33, vcc
	v_add_co_u32_e32 v44, vcc, s75, v32
	s_nop 0
	v_addc_co_u32_e32 v45, vcc, 0, v33, vcc
	v_add_co_u32_e32 v48, vcc, s64, v32
	v_mov_b32_e32 v97, v3
	s_nop 0
	v_addc_co_u32_e32 v49, vcc, 0, v33, vcc
	s_nop 0
	v_add_co_u32_e32 v52, vcc, s65, v32
	s_mov_b32 s1, s11
	s_nop 0
	v_addc_co_u32_e32 v53, vcc, 0, v33, vcc
	v_add_co_u32_e32 v32, vcc, s66, v32
	v_mov_b32_e32 v61, v3
	s_nop 0
	v_addc_co_u32_e32 v33, vcc, 0, v33, vcc
	v_lshl_add_u64 v[32:33], v[12:13], 0, s[0:1]
	v_readlane_b32 s37, v247, 42
	v_readlane_b32 s40, v247, 45
	v_readlane_b32 s41, v247, 46
	v_readlane_b32 s42, v247, 47
	v_readlane_b32 s43, v247, 48
	v_readlane_b32 s44, v247, 49
	v_readlane_b32 s45, v247, 50
	v_readlane_b32 s46, v247, 51
	v_readlane_b32 s47, v247, 52
	v_readlane_b32 s48, v247, 53
	v_readlane_b32 s49, v247, 54
	v_readlane_b32 s50, v247, 55
	v_readlane_b32 s51, v247, 56
	s_waitcnt lgkmcnt(0)
	ds_read2_b32 v[24:25], v64 offset1:16
	ds_read2_b32 v[26:27], v64 offset0:33 offset1:49
	ds_read2_b32 v[28:29], v64 offset0:66 offset1:82
	ds_read2_b32 v[30:31], v64 offset0:99 offset1:115
	ds_read2_b32 v[36:37], v64 offset0:132 offset1:148
	ds_read2_b32 v[38:39], v64 offset0:165 offset1:181
	ds_read2_b32 v[40:41], v64 offset0:198 offset1:214
	ds_read2_b32 v[42:43], v64 offset0:231 offset1:247
	ds_read2_b32 v[44:45], v85 offset0:8 offset1:24
	ds_read2_b32 v[46:47], v85 offset0:41 offset1:57
	ds_read2_b32 v[48:49], v85 offset0:74 offset1:90
	ds_read2_b32 v[50:51], v85 offset0:107 offset1:123
	s_waitcnt lgkmcnt(11)
	v_mul_f32_e32 v24, 0x42800000, v24
	s_waitcnt lgkmcnt(10)
	v_mul_f32_e32 v26, 0x42800000, v26
	s_waitcnt lgkmcnt(7)
	v_mul_f32_e32 v36, 0x42800000, v36
	s_waitcnt lgkmcnt(6)
	v_mul_f32_e32 v38, 0x42800000, v38
	v_med3_f32 v24, v24, s35, v84
	v_med3_f32 v26, v26, s35, v84
	v_med3_f32 v36, v36, s35, v84
	v_med3_f32 v38, v38, s35, v84
	v_cvt_pk_fp8_f32 v94, v24, v26
	v_cvt_pk_fp8_f32 v95, v36, v38
	v_mul_f32_e32 v28, 0x42800000, v28
	v_mul_f32_e32 v30, 0x42800000, v30
	s_waitcnt lgkmcnt(5)
	v_mul_f32_e32 v40, 0x42800000, v40
	s_waitcnt lgkmcnt(4)
	v_mul_f32_e32 v42, 0x42800000, v42
	s_waitcnt lgkmcnt(3)
	v_mul_f32_e32 v44, 0x42800000, v44
	s_waitcnt lgkmcnt(2)
	v_mul_f32_e32 v46, 0x42800000, v46
	v_med3_f32 v28, v28, s35, v84
	v_med3_f32 v30, v30, s35, v84
	v_med3_f32 v24, v40, s35, v84
	v_med3_f32 v26, v42, s35, v84
	v_cvt_pk_fp8_f32 v94, v28, v30 op_sel:[0,0,1]
	v_cvt_pk_fp8_f32 v95, v24, v26 op_sel:[0,0,1]
	v_med3_f32 v26, v44, s35, v84
	v_med3_f32 v28, v46, s35, v84
	v_cvt_pk_fp8_f32 v96, v26, v28
	ds_read2_b32 v[52:53], v85 offset0:140 offset1:156
	ds_read2_b32 v[54:55], v85 offset0:173 offset1:189
	ds_read2_b32 v[56:57], v85 offset0:206 offset1:222
	s_waitcnt lgkmcnt(4)
	v_mul_f32_e32 v48, 0x42800000, v48
	s_waitcnt lgkmcnt(3)
	v_mul_f32_e32 v24, 0x42800000, v50
	v_med3_f32 v26, v48, s35, v84
	v_med3_f32 v24, v24, s35, v84
	ds_read2_b32 v[58:59], v85 offset0:239 offset1:255
	v_cvt_pk_fp8_f32 v96, v26, v24 op_sel:[0,0,1]
	s_waitcnt lgkmcnt(3)
	v_mul_f32_e32 v24, 0x42800000, v52
	s_waitcnt lgkmcnt(2)
	v_mul_f32_e32 v26, 0x42800000, v54
	v_med3_f32 v24, v24, s35, v84
	v_med3_f32 v26, v26, s35, v84
	v_cvt_pk_fp8_f32 v97, v24, v26
	s_waitcnt lgkmcnt(1)
	v_mul_f32_e32 v28, 0x42800000, v56
	s_waitcnt lgkmcnt(0)
	v_mul_f32_e32 v24, 0x42800000, v58
	v_med3_f32 v26, v28, s35, v84
	v_med3_f32 v24, v24, s35, v84
	v_cvt_pk_fp8_f32 v97, v26, v24 op_sel:[0,0,1]
	v_or_b32_e32 v24, s7, v63
	v_lshlrev_b32_e32 v60, 12, v24
	v_mul_f32_e32 v24, 0x42800000, v25
	v_mul_f32_e32 v25, 0x42800000, v27
	v_med3_f32 v27, v24, s35, v84
	v_med3_f32 v25, v25, s35, v84
	v_mov_b32_e32 v24, v3
	v_cvt_pk_fp8_f32 v24, v27, v25
	v_mul_f32_e32 v26, 0x42800000, v29
	v_mul_f32_e32 v25, 0x42800000, v31
	v_med3_f32 v26, v26, s35, v84
	v_med3_f32 v25, v25, s35, v84
	v_cvt_pk_fp8_f32 v24, v26, v25 op_sel:[0,0,1]
	v_mul_f32_e32 v25, 0x42800000, v37
	v_mul_f32_e32 v26, 0x42800000, v39
	v_med3_f32 v28, v25, s35, v84
	v_med3_f32 v26, v26, s35, v84
	v_mov_b32_e32 v25, v3
	v_cvt_pk_fp8_f32 v25, v28, v26
	v_mul_f32_e32 v27, 0x42800000, v41
	v_mul_f32_e32 v26, 0x42800000, v43
	v_med3_f32 v27, v27, s35, v84
	v_med3_f32 v26, v26, s35, v84
	v_cvt_pk_fp8_f32 v25, v27, v26 op_sel:[0,0,1]
	v_mul_f32_e32 v26, 0x42800000, v45
	v_mul_f32_e32 v27, 0x42800000, v47
	v_med3_f32 v29, v26, s35, v84
	v_med3_f32 v27, v27, s35, v84
	v_mov_b32_e32 v26, v3
	v_cvt_pk_fp8_f32 v26, v29, v27
	v_mul_f32_e32 v28, 0x42800000, v49
	v_mul_f32_e32 v27, 0x42800000, v51
	v_med3_f32 v28, v28, s35, v84
	v_med3_f32 v27, v27, s35, v84
	v_cvt_pk_fp8_f32 v26, v28, v27 op_sel:[0,0,1]
	v_mul_f32_e32 v27, 0x42800000, v53
	v_mul_f32_e32 v28, 0x42800000, v55
	v_med3_f32 v30, v27, s35, v84
	v_med3_f32 v28, v28, s35, v84
	v_mov_b32_e32 v27, v3
	v_cvt_pk_fp8_f32 v27, v30, v28
	v_mul_f32_e32 v29, 0x42800000, v57
	v_mul_f32_e32 v28, 0x42800000, v59
	v_med3_f32 v29, v29, s35, v84
	v_med3_f32 v28, v28, s35, v84
	v_cvt_pk_fp8_f32 v27, v29, v28 op_sel:[0,0,1]
	v_or_b32_e32 v28, s7, v65
	v_lshlrev_b32_e32 v28, 12, v28
	v_mov_b32_e32 v29, v3
	v_lshl_add_u64 v[60:61], v[32:33], 0, v[60:61]
	v_lshl_add_u64 v[28:29], v[32:33], 0, v[28:29]
	global_store_dwordx4 v[60:61], v[94:97], off
	global_store_dwordx4 v[28:29], v[24:27], off
	s_waitcnt lgkmcnt(0)
	s_branch .LBB0_87

.LBB0_119:
	s_andn2_b64 vcc, exec, s[0:1]
	s_cbranch_vccnz .LBB0_121
	s_add_i32 s0, s3, 0x3e9600
	s_lshr_b32 s0, s0, 6
	s_mulk_i32 s0, 0x120
	s_and_b32 s1, s3, 63
	s_add_i32 s0, s0, s1
	s_add_i32 s0, s0, 64
	s_and_b32 s1, s0, 0xffff
	s_mul_i32 s1, s1, 0xe38f
	s_lshr_b32 s1, s1, 24
	s_mul_i32 s7, s1, 0x120
	s_sub_i32 s0, s0, s7
	v_lshl_or_b32 v24, s1, 6, v35
	s_lshl_b32 s0, s0, 5
	v_mul_u32_u24_e32 v24, 0x2400, v24
	v_readlane_b32 s36, v247, 22
	s_and_b32 s0, s0, 0xffe0
	v_lshlrev_b32_e32 v24, 2, v24
	v_mov_b32_e32 v25, v3
	v_readlane_b32 s38, v247, 24
	v_readlane_b32 s39, v247, 25
	s_lshl_b32 s10, s0, 2
	s_addk_i32 s0, 0xf800
	v_lshl_add_u64 v[24:25], s[38:39], 0, v[24:25]
	v_lshl_add_u64 v[24:25], v[24:25], 0, s[10:11]
	v_lshl_add_u64 v[32:33], v[24:25], 0, v[2:3]
	v_add_co_u32_e32 v28, vcc, s69, v32
	s_lshl_b32 s10, s1, 7
	s_nop 0
	v_addc_co_u32_e32 v29, vcc, 0, v33, vcc
	v_add_co_u32_e32 v36, vcc, s70, v32
	s_nop 0
	v_addc_co_u32_e32 v37, vcc, 0, v33, vcc
	v_add_co_u32_e32 v40, vcc, s71, v32
	v_readlane_b32 s37, v247, 23
	s_nop 0
	v_addc_co_u32_e32 v41, vcc, 0, v33, vcc
	v_add_co_u32_e32 v44, vcc, s93, v32
	s_nop 0
	v_addc_co_u32_e32 v45, vcc, 0, v33, vcc
	v_add_co_u32_e32 v48, vcc, s94, v32
	v_readlane_b32 s40, v247, 26
	s_nop 0
	v_addc_co_u32_e32 v49, vcc, 0, v33, vcc
	s_nop 0
	v_add_co_u32_e32 v52, vcc, s95, v32
	v_readlane_b32 s41, v247, 27
	s_nop 0
	v_addc_co_u32_e32 v53, vcc, 0, v33, vcc
	v_add_co_u32_e32 v32, vcc, s60, v32
	v_readlane_b32 s42, v247, 28
	s_nop 0
	v_addc_co_u32_e32 v33, vcc, 0, v33, vcc
	v_lshl_add_u64 v[32:33], v[14:15], 0, s[10:11]
	v_readlane_b32 s43, v247, 29
	v_readlane_b32 s44, v247, 30
	v_readlane_b32 s45, v247, 31
	v_readlane_b32 s46, v247, 32
	v_readlane_b32 s47, v247, 33
	v_readlane_b32 s48, v247, 34
	v_readlane_b32 s49, v247, 35
	v_readlane_b32 s50, v247, 36
	v_readlane_b32 s51, v247, 37
	s_waitcnt lgkmcnt(0)
	ds_read2_b32 v[28:29], v66 offset0:33 offset1:41
	ds_read2_b32 v[30:31], v66 offset1:8
	ds_read2_b32 v[36:37], v66 offset0:66 offset1:74
	ds_read2_b32 v[38:39], v66 offset0:99 offset1:107
	ds_read2_b32 v[40:41], v66 offset0:132 offset1:140
	ds_read2_b32 v[42:43], v66 offset0:165 offset1:173
	ds_read2_b32 v[44:45], v66 offset0:198 offset1:206
	ds_read2_b32 v[46:47], v66 offset0:231 offset1:239
	s_waitcnt lgkmcnt(7)
	v_bfe_u32 v25, v28, 16, 1
	s_waitcnt lgkmcnt(3)
	v_bfe_u32 v48, v40, 16, 1
	v_bfe_u32 v24, v30, 16, 1
	v_bfe_u32 v26, v36, 16, 1
	s_waitcnt lgkmcnt(2)
	v_bfe_u32 v49, v42, 16, 1
	s_waitcnt lgkmcnt(1)
	v_bfe_u32 v50, v44, 16, 1
	v_add3_u32 v25, v28, v25, s67
	v_add3_u32 v28, v40, v48, s67
	v_or_b32_e32 v48, s0, v35
	v_bfe_u32 v27, v38, 16, 1
	s_waitcnt lgkmcnt(0)
	v_bfe_u32 v51, v46, 16, 1
	v_add3_u32 v24, v30, v24, s67
	v_add3_u32 v26, v36, v26, s67
	v_add3_u32 v30, v42, v49, s67
	v_add3_u32 v36, v44, v50, s67
	v_ashrrev_i32_e32 v49, 31, v48
	v_add3_u32 v27, v38, v27, s67
	v_add3_u32 v38, v46, v51, s67
	v_lshrrev_b32_e32 v24, 16, v24
	v_lshrrev_b32_e32 v26, 16, v26
	v_lshrrev_b32_e32 v28, 16, v28
	v_lshrrev_b32_e32 v36, 16, v36
	v_lshlrev_b64 v[48:49], 13, v[48:49]
	v_and_or_b32 v24, v25, s68, v24
	v_and_or_b32 v25, v27, s68, v26
	v_and_or_b32 v26, v30, s68, v28
	v_and_or_b32 v27, v38, s68, v36
	v_lshl_add_u64 v[48:49], v[32:33], 0, v[48:49]
	global_store_dwordx4 v[48:49], v[24:27], off
	v_bfe_u32 v28, v47, 16, 1
	v_add3_u32 v28, v47, v28, s67
	v_bfe_u32 v24, v31, 16, 1
	v_add3_u32 v24, v31, v24, s67
	v_bfe_u32 v25, v29, 16, 1
	v_lshrrev_b32_e32 v24, 16, v24
	v_add3_u32 v25, v29, v25, s67
	v_and_or_b32 v24, v25, s68, v24
	v_bfe_u32 v25, v37, 16, 1
	v_add3_u32 v25, v37, v25, s67
	v_bfe_u32 v26, v39, 16, 1
	v_lshrrev_b32_e32 v25, 16, v25
	v_add3_u32 v26, v39, v26, s67
	v_and_or_b32 v25, v26, s68, v25
	v_bfe_u32 v26, v41, 16, 1
	v_add3_u32 v26, v41, v26, s67
	v_bfe_u32 v27, v43, 16, 1
	v_lshrrev_b32_e32 v26, 16, v26
	v_add3_u32 v27, v43, v27, s67
	v_and_or_b32 v26, v27, s68, v26
	v_bfe_u32 v27, v45, 16, 1
	v_add3_u32 v27, v45, v27, s67
	v_lshrrev_b32_e32 v27, 16, v27
	v_and_or_b32 v27, v28, s68, v27
	v_or_b32_e32 v28, s0, v67
	v_ashrrev_i32_e32 v29, 31, v28
	v_lshlrev_b64 v[28:29], 13, v[28:29]
	ds_read2_b32 v[30:31], v66 offset0:16 offset1:24
	v_lshl_add_u64 v[28:29], v[32:33], 0, v[28:29]
	global_store_dwordx4 v[28:29], v[24:27], off
	ds_read2_b32 v[28:29], v66 offset0:49 offset1:57
	ds_read2_b32 v[36:37], v66 offset0:82 offset1:90
	ds_read2_b32 v[38:39], v66 offset0:115 offset1:123
	s_waitcnt lgkmcnt(3)
	v_bfe_u32 v24, v30, 16, 1
	v_add3_u32 v24, v30, v24, s67
	s_waitcnt lgkmcnt(2)
	v_bfe_u32 v25, v28, 16, 1
	ds_read2_b32 v[40:41], v66 offset0:148 offset1:156
	v_lshrrev_b32_e32 v24, 16, v24
	v_add3_u32 v25, v28, v25, s67
	ds_read2_b32 v[42:43], v66 offset0:181 offset1:189
	v_and_or_b32 v24, v25, s68, v24
	s_waitcnt lgkmcnt(3)
	v_bfe_u32 v25, v36, 16, 1
	v_add3_u32 v25, v36, v25, s67
	s_waitcnt lgkmcnt(2)
	v_bfe_u32 v26, v38, 16, 1
	ds_read2_b32 v[44:45], v66 offset0:214 offset1:222
	v_lshrrev_b32_e32 v25, 16, v25
	v_add3_u32 v26, v38, v26, s67
	ds_read2_b32 v[46:47], v66 offset0:247 offset1:255
	v_and_or_b32 v25, v26, s68, v25
	s_waitcnt lgkmcnt(3)
	v_bfe_u32 v26, v40, 16, 1
	v_add3_u32 v26, v40, v26, s67
	s_waitcnt lgkmcnt(2)
	v_bfe_u32 v27, v42, 16, 1
	v_lshrrev_b32_e32 v26, 16, v26
	v_add3_u32 v27, v42, v27, s67
	v_and_or_b32 v26, v27, s68, v26
	s_waitcnt lgkmcnt(1)
	v_bfe_u32 v27, v44, 16, 1
	v_or_b32_e32 v48, s0, v68
	v_add3_u32 v27, v44, v27, s67
	s_waitcnt lgkmcnt(0)
	v_bfe_u32 v28, v46, 16, 1
	v_ashrrev_i32_e32 v49, 31, v48
	v_lshrrev_b32_e32 v27, 16, v27
	v_add3_u32 v28, v46, v28, s67
	v_lshlrev_b64 v[48:49], 13, v[48:49]
	v_and_or_b32 v27, v28, s68, v27
	v_lshl_add_u64 v[48:49], v[32:33], 0, v[48:49]
	global_store_dwordx4 v[48:49], v[24:27], off
	v_bfe_u32 v28, v47, 16, 1
	v_add3_u32 v28, v47, v28, s67
	v_bfe_u32 v24, v31, 16, 1
	v_add3_u32 v24, v31, v24, s67
	v_bfe_u32 v25, v29, 16, 1
	v_lshrrev_b32_e32 v24, 16, v24
	v_add3_u32 v25, v29, v25, s67
	v_and_or_b32 v24, v25, s68, v24
	v_bfe_u32 v25, v37, 16, 1
	v_add3_u32 v25, v37, v25, s67
	v_bfe_u32 v26, v39, 16, 1
	v_lshrrev_b32_e32 v25, 16, v25
	v_add3_u32 v26, v39, v26, s67
	v_and_or_b32 v25, v26, s68, v25
	v_bfe_u32 v26, v41, 16, 1
	v_add3_u32 v26, v41, v26, s67
	v_bfe_u32 v27, v43, 16, 1
	v_lshrrev_b32_e32 v26, 16, v26
	v_add3_u32 v27, v43, v27, s67
	v_and_or_b32 v26, v27, s68, v26
	v_bfe_u32 v27, v45, 16, 1
	v_add3_u32 v27, v45, v27, s67
	v_lshrrev_b32_e32 v27, 16, v27
	v_and_or_b32 v27, v28, s68, v27
	v_or_b32_e32 v28, s0, v69
	v_ashrrev_i32_e32 v29, 31, v28
	v_lshlrev_b64 v[28:29], 13, v[28:29]
	v_lshl_add_u64 v[28:29], v[32:33], 0, v[28:29]
	global_store_dwordx4 v[28:29], v[24:27], off
	s_waitcnt lgkmcnt(0)
	s_branch .LBB0_87

.LBB0_122:
	s_andn2_b64 vcc, exec, s[0:1]
	s_cbranch_vccnz .LBB0_124
	s_add_i32 s0, s3, 0xb600
	s_lshr_b32 s0, s0, 1
	s_and_b32 s0, s0, 0x7fc0
	v_or_b32_e32 v24, s0, v35
	v_readlane_b32 s36, v247, 22
	s_and_b32 s1, s14, 0xfe0
	v_lshlrev_b32_e32 v24, 14, v24
	v_mov_b32_e32 v25, v3
	v_readlane_b32 s48, v247, 34
	v_readlane_b32 s49, v247, 35
	s_lshl_b32 s10, s1, 2
	v_readlane_b32 s12, v246, 3
	v_lshl_add_u64 v[24:25], s[48:49], 0, v[24:25]
	v_lshl_add_u64 v[24:25], v[24:25], 0, s[10:11]
	v_lshl_add_u64 v[32:33], v[24:25], 0, v[2:3]
	v_add_co_u32_e32 v28, vcc, s18, v32
	v_readlane_b32 s13, v246, 4
	s_nop 0
	v_addc_co_u32_e32 v29, vcc, 0, v33, vcc
	v_add_co_u32_e32 v36, vcc, s19, v32
	s_nop 0
	v_addc_co_u32_e32 v37, vcc, 0, v33, vcc
	v_add_co_u32_e32 v40, vcc, s20, v32
	v_or_b32_e32 v87, s1, v65
	s_nop 0
	v_addc_co_u32_e32 v41, vcc, 0, v33, vcc
	v_add_co_u32_e32 v44, vcc, s21, v32
	s_nop 0
	v_addc_co_u32_e32 v45, vcc, 0, v33, vcc
	v_add_co_u32_e32 v48, vcc, s30, v32
	v_readlane_b32 s37, v247, 23
	s_nop 0
	v_addc_co_u32_e32 v49, vcc, 0, v33, vcc
	s_nop 0
	v_add_co_u32_e32 v52, vcc, s31, v32
	v_readlane_b32 s38, v247, 24
	s_nop 0
	v_addc_co_u32_e32 v53, vcc, 0, v33, vcc
	v_add_co_u32_e32 v32, vcc, s34, v32
	v_readlane_b32 s39, v247, 25
	s_nop 0
	v_addc_co_u32_e32 v33, vcc, 0, v33, vcc
	v_or_b32_e32 v32, s1, v63
	v_lshlrev_b32_e32 v33, 2, v32
	s_mov_b32 s1, s11
	v_readlane_b32 s40, v247, 26
	v_readlane_b32 s41, v247, 27
	v_readlane_b32 s42, v247, 28
	v_readlane_b32 s43, v247, 29
	v_readlane_b32 s44, v247, 30
	v_readlane_b32 s45, v247, 31
	v_readlane_b32 s46, v247, 32
	v_readlane_b32 s47, v247, 33
	v_readlane_b32 s50, v247, 36
	v_readlane_b32 s51, v247, 37
	s_waitcnt lgkmcnt(0)
	v_mov_b32_e32 v44, v234
	v_lshlrev_b32_e32 v24, 2, v87
	v_mov_b32_e32 v91, v235
	v_lshl_add_u64 v[24:25], v[16:17], 0, s[0:1]
	v_mov_b32_e32 v27, v3
	v_lshlrev_b32_e32 v26, 12, v32
	v_lshl_add_u64 v[48:49], v[24:25], 0, v[26:27]
	ds_read2_b32 v[50:51], v64 offset1:16
	ds_read2_b32 v[52:53], v64 offset0:33 offset1:49
	ds_read2_b32 v[54:55], v64 offset0:66 offset1:82
	ds_read2_b32 v[56:57], v64 offset0:99 offset1:115
	ds_read2_b32 v[58:59], v64 offset0:132 offset1:148
	ds_read2_b32 v[60:61], v64 offset0:165 offset1:181
	ds_read2_b32 v[88:89], v64 offset0:198 offset1:214
	ds_read2_b32 v[94:95], v64 offset0:231 offset1:247
	ds_read2_b32 v[36:37], v85 offset0:8 offset1:24
	ds_read2_b32 v[38:39], v85 offset0:41 offset1:57
	ds_read2_b32 v[40:41], v85 offset0:74 offset1:90
	ds_read2_b32 v[42:43], v85 offset0:107 offset1:123
	ds_read2_b32 v[26:27], v85 offset0:140 offset1:156
	ds_read2_b32 v[28:29], v85 offset0:173 offset1:189
	ds_read2_b32 v[30:31], v85 offset0:206 offset1:222
	ds_read2_b32 v[32:33], v85 offset0:239 offset1:255
	v_div_scale_f32 v45, s[0:1], v44, v44, s61
	v_rcp_f32_e32 v47, v45
	v_div_scale_f32 v46, vcc, s61, v44, s61
	v_div_scale_f32 v93, s[0:1], v91, v91, s61
	v_fma_f32 v98, -v45, v47, 1.0
	v_fmac_f32_e32 v47, v98, v47
	v_mul_f32_e32 v98, v46, v47
	v_fma_f32 v100, -v45, v98, v46
	v_fmac_f32_e32 v98, v100, v47
	v_fma_f32 v45, -v45, v98, v46
	v_div_fmas_f32 v45, v45, v47, v98
	v_div_fixup_f32 v45, v45, v44, s61
	v_cmp_lt_f32_e32 vcc, 0, v44
	v_rcp_f32_e32 v96, v93
	v_div_scale_f32 v97, s[0:1], s61, v91, s61
	v_cndmask_b32_e32 v44, 0, v45, vcc
	s_waitcnt lgkmcnt(14)
	v_mul_f32_e32 v45, v50, v44
	v_mul_f32_e32 v46, v52, v44
	s_waitcnt lgkmcnt(2)
	v_mul_f32_e32 v28, v44, v28
	v_mul_f32_e32 v47, v44, v54
	v_mul_f32_e32 v50, v44, v56
	v_mul_f32_e32 v52, v44, v58
	v_mul_f32_e32 v54, v44, v60
	v_mul_f32_e32 v56, v44, v88
	v_mul_f32_e32 v58, v44, v94
	v_mul_f32_e32 v36, v44, v36
	v_mul_f32_e32 v38, v44, v38
	v_mul_f32_e32 v40, v44, v40
	v_mul_f32_e32 v42, v44, v42
	v_mul_f32_e32 v26, v44, v26
	s_waitcnt lgkmcnt(1)
	v_mul_f32_e32 v30, v44, v30
	s_waitcnt lgkmcnt(0)
	v_mul_f32_e32 v32, v44, v32
	v_med3_f32 v44, v45, s62, v86
	v_med3_f32 v45, v46, s62, v86
	v_med3_f32 v28, v28, s62, v86
	v_med3_f32 v46, v47, s62, v86
	v_med3_f32 v26, v26, s62, v86
	v_med3_f32 v30, v30, s62, v86
	v_rndne_f32_e32 v45, v45
	v_rndne_f32_e32 v28, v28
	v_med3_f32 v47, v50, s62, v86
	v_med3_f32 v32, v32, s62, v86
	v_rndne_f32_e32 v44, v44
	v_rndne_f32_e32 v46, v46
	v_rndne_f32_e32 v26, v26
	v_rndne_f32_e32 v30, v30
	v_cvt_i32_f32_e32 v45, v45
	v_cvt_i32_f32_e32 v28, v28
	v_fma_f32 v99, -v93, v96, 1.0
	v_rndne_f32_e32 v47, v47
	v_rndne_f32_e32 v32, v32
	v_cvt_i32_f32_e32 v44, v44
	v_cvt_i32_f32_sdwa v46, v46 dst_sel:WORD_1 dst_unused:UNUSED_PAD src0_sel:DWORD
	v_cvt_i32_f32_e32 v26, v26
	v_cvt_i32_f32_sdwa v30, v30 dst_sel:WORD_1 dst_unused:UNUSED_PAD src0_sel:DWORD
	v_fmac_f32_e32 v96, v99, v96
	v_cvt_i32_f32_sdwa v47, v47 dst_sel:BYTE_3 dst_unused:UNUSED_PAD src0_sel:DWORD
	v_cvt_i32_f32_sdwa v32, v32 dst_sel:BYTE_3 dst_unused:UNUSED_PAD src0_sel:DWORD
	v_mul_f32_e32 v99, v97, v96
	v_fma_f32 v101, -v93, v99, v97
	v_med3_f32 v38, v38, s62, v86
	v_lshlrev_b32_e32 v45, 8, v45
	v_lshlrev_b32_e32 v28, 8, v28
	v_med3_f32 v36, v36, s62, v86
	v_med3_f32 v40, v40, s62, v86
	v_rndne_f32_e32 v38, v38
	v_and_b32_e32 v46, 0xff0000, v46
	v_and_b32_e32 v30, 0xff0000, v30
	v_perm_b32 v44, v45, v44, s63
	v_perm_b32 v26, v28, v26, s63
	v_fmac_f32_e32 v99, v101, v96
	v_med3_f32 v42, v42, s62, v86
	v_rndne_f32_e32 v36, v36
	v_rndne_f32_e32 v40, v40
	v_cvt_i32_f32_e32 v38, v38
	v_or3_b32 v44, v44, v46, v47
	v_or3_b32 v47, v26, v30, v32
	v_fma_f32 v26, -v93, v99, v97
	s_mov_b64 vcc, s[0:1]
	v_rndne_f32_e32 v42, v42
	v_cvt_i32_f32_e32 v36, v36
	v_cvt_i32_f32_sdwa v40, v40 dst_sel:WORD_1 dst_unused:UNUSED_PAD src0_sel:DWORD
	v_div_fmas_f32 v26, v26, v96, v99
	v_cvt_i32_f32_sdwa v42, v42 dst_sel:BYTE_3 dst_unused:UNUSED_PAD src0_sel:DWORD
	v_div_fixup_f32 v26, v26, v91, s61
	v_cmp_lt_f32_e32 vcc, 0, v91
	v_med3_f32 v50, v52, s62, v86
	v_med3_f32 v52, v54, s62, v86
	v_cndmask_b32_e32 v26, 0, v26, vcc
	v_lshlrev_b32_e32 v38, 8, v38
	v_mul_f32_e32 v30, v53, v26
	v_med3_f32 v54, v56, s62, v86
	v_rndne_f32_e32 v52, v52
	v_and_b32_e32 v40, 0xff0000, v40
	v_perm_b32 v36, v38, v36, s63
	v_mul_f32_e32 v28, v51, v26
	v_mul_f32_e32 v32, v26, v55
	v_med3_f32 v30, v30, s62, v86
	v_med3_f32 v56, v58, s62, v86
	v_rndne_f32_e32 v50, v50
	v_rndne_f32_e32 v54, v54
	v_cvt_i32_f32_e32 v52, v52
	v_or3_b32 v46, v36, v40, v42
	v_mul_f32_e32 v36, v26, v57
	v_med3_f32 v28, v28, s62, v86
	v_rndne_f32_e32 v30, v30
	v_med3_f32 v32, v32, s62, v86
	v_rndne_f32_e32 v56, v56
	v_cvt_i32_f32_e32 v50, v50
	v_cvt_i32_f32_sdwa v54, v54 dst_sel:WORD_1 dst_unused:UNUSED_PAD src0_sel:DWORD
	v_rndne_f32_e32 v28, v28
	v_cvt_i32_f32_e32 v30, v30
	v_rndne_f32_e32 v32, v32
	v_med3_f32 v36, v36, s62, v86
	v_cvt_i32_f32_sdwa v56, v56 dst_sel:BYTE_3 dst_unused:UNUSED_PAD src0_sel:DWORD
	v_cvt_i32_f32_e32 v28, v28
	v_cvt_i32_f32_sdwa v32, v32 dst_sel:WORD_1 dst_unused:UNUSED_PAD src0_sel:DWORD
	v_rndne_f32_e32 v36, v36
	v_cvt_i32_f32_sdwa v36, v36 dst_sel:BYTE_3 dst_unused:UNUSED_PAD src0_sel:DWORD
	v_lshlrev_b32_e32 v52, 8, v52
	v_and_b32_e32 v54, 0xff0000, v54
	v_perm_b32 v45, v52, v50, s63
	v_lshlrev_b32_e32 v30, 8, v30
	v_or3_b32 v45, v45, v54, v56
	v_perm_b32 v28, v30, v28, s63
	v_and_b32_e32 v30, 0xff0000, v32
	global_store_dwordx4 v[48:49], v[44:47], off
	v_mul_f32_e32 v32, v26, v89
	v_med3_f32 v32, v32, s62, v86
	v_or3_b32 v44, v28, v30, v36
	v_mul_f32_e32 v30, v26, v61
	v_mul_f32_e32 v28, v26, v59
	v_med3_f32 v30, v30, s62, v86
	v_mul_f32_e32 v36, v26, v95
	v_med3_f32 v28, v28, s62, v86
	v_rndne_f32_e32 v30, v30
	v_rndne_f32_e32 v28, v28
	v_cvt_i32_f32_e32 v30, v30
	v_rndne_f32_e32 v32, v32
	v_med3_f32 v36, v36, s62, v86
	v_cvt_i32_f32_e32 v28, v28
	v_cvt_i32_f32_sdwa v32, v32 dst_sel:WORD_1 dst_unused:UNUSED_PAD src0_sel:DWORD
	v_rndne_f32_e32 v36, v36
	v_cvt_i32_f32_sdwa v36, v36 dst_sel:BYTE_3 dst_unused:UNUSED_PAD src0_sel:DWORD
	v_lshlrev_b32_e32 v30, 8, v30
	v_perm_b32 v28, v30, v28, s63
	v_and_b32_e32 v30, 0xff0000, v32
	v_or3_b32 v45, v28, v30, v36
	v_mul_f32_e32 v30, v26, v39
	v_mul_f32_e32 v28, v26, v37
	v_mul_f32_e32 v32, v26, v41
	v_med3_f32 v30, v30, s62, v86
	v_mul_f32_e32 v36, v26, v43
	v_med3_f32 v28, v28, s62, v86
	v_rndne_f32_e32 v30, v30
	v_med3_f32 v32, v32, s62, v86
	v_rndne_f32_e32 v28, v28
	v_cvt_i32_f32_e32 v30, v30
	v_rndne_f32_e32 v32, v32
	v_med3_f32 v36, v36, s62, v86
	v_cvt_i32_f32_e32 v28, v28
	v_cvt_i32_f32_sdwa v32, v32 dst_sel:WORD_1 dst_unused:UNUSED_PAD src0_sel:DWORD
	v_rndne_f32_e32 v36, v36
	v_cvt_i32_f32_sdwa v36, v36 dst_sel:BYTE_3 dst_unused:UNUSED_PAD src0_sel:DWORD
	v_lshlrev_b32_e32 v30, 8, v30
	v_perm_b32 v28, v30, v28, s63
	v_and_b32_e32 v30, 0xff0000, v32
	v_or3_b32 v46, v28, v30, v36
	v_mul_f32_e32 v28, v26, v29
	v_mul_f32_e32 v27, v26, v27
	v_mul_f32_e32 v29, v26, v31
	v_med3_f32 v28, v28, s62, v86
	v_mul_f32_e32 v26, v26, v33
	v_med3_f32 v27, v27, s62, v86
	v_rndne_f32_e32 v28, v28
	v_med3_f32 v29, v29, s62, v86
	v_rndne_f32_e32 v27, v27
	v_cvt_i32_f32_e32 v28, v28
	v_rndne_f32_e32 v29, v29
	v_med3_f32 v26, v26, s62, v86
	v_cvt_i32_f32_e32 v27, v27
	v_cvt_i32_f32_sdwa v29, v29 dst_sel:WORD_1 dst_unused:UNUSED_PAD src0_sel:DWORD
	v_rndne_f32_e32 v26, v26
	v_cvt_i32_f32_sdwa v26, v26 dst_sel:BYTE_3 dst_unused:UNUSED_PAD src0_sel:DWORD
	v_lshlrev_b32_e32 v28, 8, v28
	v_perm_b32 v27, v28, v27, s63
	v_and_b32_e32 v28, 0xff0000, v29
	v_or3_b32 v47, v27, v28, v26
	v_lshlrev_b32_e32 v26, 12, v87
	v_mov_b32_e32 v27, v3
	v_lshl_add_u64 v[24:25], v[24:25], 0, v[26:27]
	global_store_dwordx4 v[24:25], v[44:47], off
	s_waitcnt lgkmcnt(0)
	s_branch .LBB0_87

.LBB0_125:
	s_andn2_b64 vcc, exec, s[0:1]
	s_cbranch_vccnz .LBB0_127
	s_add_i32 s0, s3, 0xfe00
	s_and_b32 s1, s0, 0xffff
	s_mul_i32 s1, s1, 0xe38f
	s_lshr_b32 s1, s1, 24
	s_mul_i32 s7, s1, 0x120
	s_sub_i32 s7, s0, s7
	s_lshl_b32 s0, s1, 6
	v_or_b32_e32 v24, s0, v35
	s_lshl_b32 s1, s7, 5
	v_mul_u32_u24_e32 v24, 0x2400, v24
	v_readlane_b32 s36, v247, 22
	s_and_b32 s1, s1, 0xffe0
	v_lshlrev_b32_e32 v24, 2, v24
	v_mov_b32_e32 v25, v3
	v_readlane_b32 s38, v247, 24
	v_readlane_b32 s39, v247, 25
	s_lshl_b32 s10, s1, 2
	v_or_b32_e32 v87, s1, v65
	v_lshl_add_u64 v[24:25], s[38:39], 0, v[24:25]
	v_lshl_add_u64 v[24:25], v[24:25], 0, s[10:11]
	v_lshl_add_u64 v[32:33], v[24:25], 0, v[2:3]
	v_add_co_u32_e32 v28, vcc, s69, v32
	v_readlane_b32 s37, v247, 23
	s_nop 0
	v_addc_co_u32_e32 v29, vcc, 0, v33, vcc
	v_add_co_u32_e32 v36, vcc, s70, v32
	s_nop 0
	v_addc_co_u32_e32 v37, vcc, 0, v33, vcc
	v_add_co_u32_e32 v40, vcc, s71, v32
	v_readlane_b32 s40, v247, 26
	s_nop 0
	v_addc_co_u32_e32 v41, vcc, 0, v33, vcc
	v_add_co_u32_e32 v44, vcc, s93, v32
	s_nop 0
	v_addc_co_u32_e32 v45, vcc, 0, v33, vcc
	v_add_co_u32_e32 v48, vcc, s94, v32
	v_readlane_b32 s41, v247, 27
	s_nop 0
	v_addc_co_u32_e32 v49, vcc, 0, v33, vcc
	s_nop 0
	v_add_co_u32_e32 v52, vcc, s95, v32
	v_readlane_b32 s42, v247, 28
	s_nop 0
	v_addc_co_u32_e32 v53, vcc, 0, v33, vcc
	v_add_co_u32_e32 v32, vcc, s60, v32
	v_readlane_b32 s43, v247, 29
	s_nop 0
	v_addc_co_u32_e32 v33, vcc, 0, v33, vcc
	v_or_b32_e32 v32, s1, v63
	v_lshlrev_b32_e32 v33, 2, v32
	s_mov_b32 s1, s11
	v_readlane_b32 s44, v247, 30
	v_readlane_b32 s45, v247, 31
	v_readlane_b32 s46, v247, 32
	v_readlane_b32 s47, v247, 33
	v_readlane_b32 s48, v247, 34
	v_readlane_b32 s49, v247, 35
	v_readlane_b32 s50, v247, 36
	v_readlane_b32 s51, v247, 37
	s_waitcnt lgkmcnt(0)
	v_mov_b32_e32 v26, v234
	v_lshlrev_b32_e32 v24, 2, v87
	v_mov_b32_e32 v91, v235
	v_mov_b32_e32 v25, v3
	v_lshl_add_u64 v[28:29], v[18:19], 0, s[0:1]
	v_lshlrev_b32_e32 v24, 12, v32
	v_lshl_add_u64 v[30:31], v[28:29], 0, v[24:25]
	ds_read2_b32 v[32:33], v64 offset1:16
	ds_read2_b32 v[36:37], v64 offset0:33 offset1:49
	ds_read2_b32 v[38:39], v64 offset0:66 offset1:82
	ds_read2_b32 v[40:41], v64 offset0:99 offset1:115
	ds_read2_b32 v[42:43], v64 offset0:132 offset1:148
	ds_read2_b32 v[44:45], v64 offset0:165 offset1:181
	ds_read2_b32 v[46:47], v64 offset0:198 offset1:214
	ds_read2_b32 v[48:49], v64 offset0:231 offset1:247
	ds_read2_b32 v[50:51], v85 offset0:8 offset1:24
	ds_read2_b32 v[52:53], v85 offset0:41 offset1:57
	ds_read2_b32 v[54:55], v85 offset0:74 offset1:90
	ds_read2_b32 v[56:57], v85 offset0:107 offset1:123
	ds_read2_b32 v[58:59], v85 offset0:140 offset1:156
	ds_read2_b32 v[60:61], v85 offset0:173 offset1:189
	ds_read2_b32 v[88:89], v85 offset0:206 offset1:222
	ds_read2_b32 v[94:95], v85 offset0:239 offset1:255
	v_div_scale_f32 v24, s[0:1], v26, v26, s61
	v_rcp_f32_e32 v25, v24
	v_div_scale_f32 v93, s[0:1], v91, v91, s61
	v_rcp_f32_e32 v96, v93
	v_fma_f32 v97, -v24, v25, 1.0
	v_div_scale_f32 v27, vcc, s61, v26, s61
	v_fmac_f32_e32 v25, v97, v25
	v_fma_f32 v98, -v93, v96, 1.0
	v_mul_f32_e32 v97, v27, v25
	v_fmac_f32_e32 v96, v98, v96
	v_fma_f32 v98, -v24, v97, v27
	v_fmac_f32_e32 v97, v98, v25
	v_fma_f32 v24, -v24, v97, v27
	v_div_fmas_f32 v24, v24, v25, v97
	v_div_fixup_f32 v24, v24, v26, s61
	v_cmp_lt_f32_e32 vcc, 0, v26
	s_nop 1
	v_cndmask_b32_e32 v24, 0, v24, vcc
	s_waitcnt lgkmcnt(14)
	v_mul_f32_e32 v25, v32, v24
	v_mul_f32_e32 v26, v36, v24
	s_waitcnt lgkmcnt(13)
	v_mul_f32_e32 v27, v24, v38
	s_waitcnt lgkmcnt(12)
	v_mul_f32_e32 v32, v24, v40
	s_waitcnt lgkmcnt(11)
	v_mul_f32_e32 v36, v24, v42
	s_waitcnt lgkmcnt(10)
	v_mul_f32_e32 v38, v24, v44
	s_waitcnt lgkmcnt(9)
	v_mul_f32_e32 v40, v24, v46
	s_waitcnt lgkmcnt(8)
	v_mul_f32_e32 v42, v24, v48
	s_waitcnt lgkmcnt(6)
	v_mul_f32_e32 v46, v24, v52
	s_waitcnt lgkmcnt(5)
	v_mul_f32_e32 v48, v24, v54
	s_waitcnt lgkmcnt(2)
	v_mul_f32_e32 v54, v24, v60
	v_mul_f32_e32 v44, v24, v50
	v_mul_f32_e32 v50, v24, v56
	v_mul_f32_e32 v52, v24, v58
	s_waitcnt lgkmcnt(1)
	v_mul_f32_e32 v56, v24, v88
	v_med3_f32 v26, v26, s62, v86
	v_med3_f32 v27, v27, s62, v86
	v_med3_f32 v38, v38, s62, v86
	v_med3_f32 v40, v40, s62, v86
	v_med3_f32 v46, v46, s62, v86
	v_med3_f32 v48, v48, s62, v86
	v_med3_f32 v54, v54, s62, v86
	s_waitcnt lgkmcnt(0)
	v_mul_f32_e32 v24, v24, v94
	v_med3_f32 v25, v25, s62, v86
	v_med3_f32 v36, v36, s62, v86
	v_med3_f32 v44, v44, s62, v86
	v_med3_f32 v52, v52, s62, v86
	v_med3_f32 v56, v56, s62, v86
	v_rndne_f32_e32 v26, v26
	v_rndne_f32_e32 v27, v27
	v_rndne_f32_e32 v38, v38
	v_rndne_f32_e32 v40, v40
	v_rndne_f32_e32 v46, v46
	v_rndne_f32_e32 v48, v48
	v_rndne_f32_e32 v54, v54
	v_med3_f32 v32, v32, s62, v86
	v_med3_f32 v42, v42, s62, v86
	v_med3_f32 v50, v50, s62, v86
	v_med3_f32 v24, v24, s62, v86
	v_rndne_f32_e32 v25, v25
	v_rndne_f32_e32 v36, v36
	v_rndne_f32_e32 v44, v44
	v_rndne_f32_e32 v52, v52
	v_rndne_f32_e32 v56, v56
	v_cvt_i32_f32_e32 v26, v26
	v_cvt_i32_f32_sdwa v27, v27 dst_sel:WORD_1 dst_unused:UNUSED_PAD src0_sel:DWORD
	v_cvt_i32_f32_e32 v38, v38
	v_cvt_i32_f32_sdwa v40, v40 dst_sel:WORD_1 dst_unused:UNUSED_PAD src0_sel:DWORD
	v_cvt_i32_f32_e32 v46, v46
	v_cvt_i32_f32_sdwa v48, v48 dst_sel:WORD_1 dst_unused:UNUSED_PAD src0_sel:DWORD
	v_cvt_i32_f32_e32 v54, v54
	v_rndne_f32_e32 v32, v32
	v_rndne_f32_e32 v42, v42
	v_rndne_f32_e32 v50, v50
	v_rndne_f32_e32 v24, v24
	v_cvt_i32_f32_e32 v25, v25
	v_cvt_i32_f32_e32 v36, v36
	v_cvt_i32_f32_e32 v44, v44
	v_cvt_i32_f32_e32 v52, v52
	v_cvt_i32_f32_sdwa v56, v56 dst_sel:WORD_1 dst_unused:UNUSED_PAD src0_sel:DWORD
	v_cvt_i32_f32_sdwa v32, v32 dst_sel:BYTE_3 dst_unused:UNUSED_PAD src0_sel:DWORD
	v_cvt_i32_f32_sdwa v42, v42 dst_sel:BYTE_3 dst_unused:UNUSED_PAD src0_sel:DWORD
	v_cvt_i32_f32_sdwa v50, v50 dst_sel:BYTE_3 dst_unused:UNUSED_PAD src0_sel:DWORD
	v_cvt_i32_f32_sdwa v58, v24 dst_sel:BYTE_3 dst_unused:UNUSED_PAD src0_sel:DWORD
	v_lshlrev_b32_e32 v24, 8, v26
	v_and_b32_e32 v26, 0xff0000, v27
	v_lshlrev_b32_e32 v27, 8, v38
	v_and_b32_e32 v38, 0xff0000, v40
	v_lshlrev_b32_e32 v40, 8, v46
	v_and_b32_e32 v46, 0xff0000, v48
	v_lshlrev_b32_e32 v48, 8, v54
	v_and_b32_e32 v54, 0xff0000, v56
	v_perm_b32 v24, v24, v25, s63
	v_perm_b32 v25, v27, v36, s63
	v_perm_b32 v27, v40, v44, s63
	v_perm_b32 v36, v48, v52, s63
	v_or3_b32 v24, v24, v26, v32
	v_or3_b32 v25, v25, v38, v42
	v_or3_b32 v26, v27, v46, v50
	v_or3_b32 v27, v36, v54, v58
	global_store_dwordx4 v[30:31], v[24:27], off
	s_nop 1
	v_div_scale_f32 v24, vcc, s61, v91, s61
	v_mul_f32_e32 v25, v24, v96
	v_fma_f32 v26, -v93, v25, v24
	v_fmac_f32_e32 v25, v26, v96
	v_fma_f32 v24, -v93, v25, v24
	v_div_fmas_f32 v24, v24, v96, v25
	v_div_fixup_f32 v24, v24, v91, s61
	v_cmp_lt_f32_e32 vcc, 0, v91
	s_nop 1
	v_cndmask_b32_e32 v27, 0, v24, vcc
	v_mul_f32_e32 v25, v37, v27
	v_mul_f32_e32 v24, v33, v27
	v_mul_f32_e32 v26, v27, v39
	v_med3_f32 v25, v25, s62, v86
	v_mul_f32_e32 v30, v27, v41
	v_med3_f32 v24, v24, s62, v86
	v_rndne_f32_e32 v25, v25
	v_med3_f32 v26, v26, s62, v86
	v_rndne_f32_e32 v24, v24
	v_cvt_i32_f32_e32 v25, v25
	v_rndne_f32_e32 v26, v26
	v_med3_f32 v30, v30, s62, v86
	v_cvt_i32_f32_e32 v24, v24
	v_cvt_i32_f32_sdwa v26, v26 dst_sel:WORD_1 dst_unused:UNUSED_PAD src0_sel:DWORD
	v_rndne_f32_e32 v30, v30
	v_cvt_i32_f32_sdwa v30, v30 dst_sel:BYTE_3 dst_unused:UNUSED_PAD src0_sel:DWORD
	v_lshlrev_b32_e32 v25, 8, v25
	v_perm_b32 v24, v25, v24, s63
	v_and_b32_e32 v25, 0xff0000, v26
	v_mul_f32_e32 v26, v27, v45
	v_or3_b32 v24, v24, v25, v30
	v_mul_f32_e32 v25, v27, v43
	v_mul_f32_e32 v30, v27, v47
	v_med3_f32 v26, v26, s62, v86
	v_mul_f32_e32 v31, v27, v49
	v_med3_f32 v25, v25, s62, v86
	v_rndne_f32_e32 v26, v26
	v_med3_f32 v30, v30, s62, v86
	v_rndne_f32_e32 v25, v25
	v_cvt_i32_f32_e32 v26, v26
	v_rndne_f32_e32 v30, v30
	v_med3_f32 v31, v31, s62, v86
	v_cvt_i32_f32_e32 v25, v25
	v_cvt_i32_f32_sdwa v30, v30 dst_sel:WORD_1 dst_unused:UNUSED_PAD src0_sel:DWORD
	v_rndne_f32_e32 v31, v31
	v_cvt_i32_f32_sdwa v31, v31 dst_sel:BYTE_3 dst_unused:UNUSED_PAD src0_sel:DWORD
	v_lshlrev_b32_e32 v26, 8, v26
	v_perm_b32 v25, v26, v25, s63
	v_and_b32_e32 v26, 0xff0000, v30
	v_mul_f32_e32 v30, v27, v53
	v_or3_b32 v25, v25, v26, v31
	v_mul_f32_e32 v26, v27, v51
	v_mul_f32_e32 v31, v27, v55
	v_med3_f32 v30, v30, s62, v86
	v_mul_f32_e32 v32, v27, v57
	v_med3_f32 v26, v26, s62, v86
	v_rndne_f32_e32 v30, v30
	v_med3_f32 v31, v31, s62, v86
	v_rndne_f32_e32 v26, v26
	v_cvt_i32_f32_e32 v30, v30
	v_rndne_f32_e32 v31, v31
	v_med3_f32 v32, v32, s62, v86
	v_cvt_i32_f32_e32 v26, v26
	v_cvt_i32_f32_sdwa v31, v31 dst_sel:WORD_1 dst_unused:UNUSED_PAD src0_sel:DWORD
	v_rndne_f32_e32 v32, v32
	v_cvt_i32_f32_sdwa v32, v32 dst_sel:BYTE_3 dst_unused:UNUSED_PAD src0_sel:DWORD
	v_lshlrev_b32_e32 v30, 8, v30
	v_perm_b32 v26, v30, v26, s63
	v_and_b32_e32 v30, 0xff0000, v31
	v_mul_f32_e32 v31, v27, v61
	v_or3_b32 v26, v26, v30, v32
	v_mul_f32_e32 v30, v27, v59
	v_mul_f32_e32 v32, v27, v89
	v_med3_f32 v31, v31, s62, v86
	v_mul_f32_e32 v27, v27, v95
	v_med3_f32 v30, v30, s62, v86
	v_rndne_f32_e32 v31, v31
	v_med3_f32 v32, v32, s62, v86
	v_rndne_f32_e32 v30, v30
	v_cvt_i32_f32_e32 v31, v31
	v_rndne_f32_e32 v32, v32
	v_med3_f32 v27, v27, s62, v86
	v_cvt_i32_f32_e32 v30, v30
	v_cvt_i32_f32_sdwa v32, v32 dst_sel:WORD_1 dst_unused:UNUSED_PAD src0_sel:DWORD
	v_rndne_f32_e32 v27, v27
	v_cvt_i32_f32_sdwa v27, v27 dst_sel:BYTE_3 dst_unused:UNUSED_PAD src0_sel:DWORD
	v_lshlrev_b32_e32 v31, 8, v31
	v_perm_b32 v30, v31, v30, s63
	v_and_b32_e32 v31, 0xff0000, v32
	v_or3_b32 v27, v30, v31, v27
	v_lshlrev_b32_e32 v30, 12, v87
	v_mov_b32_e32 v31, v3
	v_lshl_add_u64 v[28:29], v[28:29], 0, v[30:31]
	global_store_dwordx4 v[28:29], v[24:27], off
	s_waitcnt lgkmcnt(0)
	s_branch .LBB0_87

.LBB0_128:
	s_andn2_b64 vcc, exec, s[0:1]
	s_cbranch_vccnz .LBB0_130
	s_add_i32 s0, s3, 0x5400
	s_lshr_b32 s0, s0, 1
	s_and_b32 s0, s0, 0x7fc0
	s_lshl_b32 s1, s3, 5
	v_or_b32_e32 v24, s0, v35
	v_readlane_b32 s36, v247, 6
	s_and_b32 s7, s1, 0xfe0
	v_lshlrev_b32_e32 v24, 14, v24
	v_mov_b32_e32 v25, v3
	v_readlane_b32 s50, v247, 20
	v_readlane_b32 s51, v247, 21
	s_lshl_b32 s10, s7, 2
	v_mov_b32_e32 v94, v3
	v_lshl_add_u64 v[24:25], s[50:51], 0, v[24:25]
	v_lshl_add_u64 v[24:25], v[24:25], 0, s[10:11]
	v_lshl_add_u64 v[32:33], v[24:25], 0, v[2:3]
	v_add_co_u32_e32 v28, vcc, s18, v32
	v_mov_b32_e32 v95, v3
	s_nop 0
	v_addc_co_u32_e32 v29, vcc, 0, v33, vcc
	v_add_co_u32_e32 v36, vcc, s19, v32
	s_nop 0
	v_addc_co_u32_e32 v37, vcc, 0, v33, vcc
	v_add_co_u32_e32 v40, vcc, s20, v32
	v_mov_b32_e32 v96, v3
	s_nop 0
	v_addc_co_u32_e32 v41, vcc, 0, v33, vcc
	v_add_co_u32_e32 v44, vcc, s21, v32
	s_nop 0
	v_addc_co_u32_e32 v45, vcc, 0, v33, vcc
	v_add_co_u32_e32 v48, vcc, s30, v32
	v_mov_b32_e32 v97, v3
	s_nop 0
	v_addc_co_u32_e32 v49, vcc, 0, v33, vcc
	s_nop 0
	v_add_co_u32_e32 v52, vcc, s31, v32
	s_mov_b32 s1, s11
	s_nop 0
	v_addc_co_u32_e32 v53, vcc, 0, v33, vcc
	v_add_co_u32_e32 v32, vcc, s34, v32
	v_mov_b32_e32 v61, v3
	s_nop 0
	v_addc_co_u32_e32 v33, vcc, 0, v33, vcc
	v_lshl_add_u64 v[32:33], v[20:21], 0, s[0:1]
	v_readlane_b32 s37, v247, 7
	v_readlane_b32 s38, v247, 8
	v_readlane_b32 s39, v247, 9
	v_readlane_b32 s40, v247, 10
	v_readlane_b32 s41, v247, 11
	v_readlane_b32 s42, v247, 12
	v_readlane_b32 s43, v247, 13
	v_readlane_b32 s44, v247, 14
	v_readlane_b32 s45, v247, 15
	v_readlane_b32 s46, v247, 16
	v_readlane_b32 s47, v247, 17
	v_readlane_b32 s48, v247, 18
	v_readlane_b32 s49, v247, 19
	s_waitcnt lgkmcnt(0)
	ds_read2_b32 v[24:25], v64 offset1:16
	ds_read2_b32 v[26:27], v64 offset0:33 offset1:49
	ds_read2_b32 v[28:29], v64 offset0:66 offset1:82
	ds_read2_b32 v[30:31], v64 offset0:99 offset1:115
	ds_read2_b32 v[36:37], v64 offset0:132 offset1:148
	ds_read2_b32 v[38:39], v64 offset0:165 offset1:181
	ds_read2_b32 v[40:41], v64 offset0:198 offset1:214
	ds_read2_b32 v[42:43], v64 offset0:231 offset1:247
	ds_read2_b32 v[44:45], v85 offset0:8 offset1:24
	ds_read2_b32 v[46:47], v85 offset0:41 offset1:57
	ds_read2_b32 v[48:49], v85 offset0:74 offset1:90
	ds_read2_b32 v[50:51], v85 offset0:107 offset1:123
	s_waitcnt lgkmcnt(11)
	v_mul_f32_e32 v24, 0x43000000, v24
	s_waitcnt lgkmcnt(10)
	v_mul_f32_e32 v26, 0x43000000, v26
	s_waitcnt lgkmcnt(7)
	v_mul_f32_e32 v36, 0x43000000, v36
	s_waitcnt lgkmcnt(6)
	v_mul_f32_e32 v38, 0x43000000, v38
	v_med3_f32 v24, v24, s35, v84
	v_med3_f32 v26, v26, s35, v84
	v_med3_f32 v36, v36, s35, v84
	v_med3_f32 v38, v38, s35, v84
	v_cvt_pk_fp8_f32 v94, v24, v26
	v_cvt_pk_fp8_f32 v95, v36, v38
	v_mul_f32_e32 v28, 0x43000000, v28
	v_mul_f32_e32 v30, 0x43000000, v30
	s_waitcnt lgkmcnt(5)
	v_mul_f32_e32 v40, 0x43000000, v40
	s_waitcnt lgkmcnt(4)
	v_mul_f32_e32 v42, 0x43000000, v42
	s_waitcnt lgkmcnt(3)
	v_mul_f32_e32 v44, 0x43000000, v44
	s_waitcnt lgkmcnt(2)
	v_mul_f32_e32 v46, 0x43000000, v46
	v_med3_f32 v28, v28, s35, v84
	v_med3_f32 v30, v30, s35, v84
	v_med3_f32 v24, v40, s35, v84
	v_med3_f32 v26, v42, s35, v84
	v_cvt_pk_fp8_f32 v94, v28, v30 op_sel:[0,0,1]
	v_cvt_pk_fp8_f32 v95, v24, v26 op_sel:[0,0,1]
	v_med3_f32 v26, v44, s35, v84
	v_med3_f32 v28, v46, s35, v84
	v_cvt_pk_fp8_f32 v96, v26, v28
	ds_read2_b32 v[52:53], v85 offset0:140 offset1:156
	ds_read2_b32 v[54:55], v85 offset0:173 offset1:189
	ds_read2_b32 v[56:57], v85 offset0:206 offset1:222
	s_waitcnt lgkmcnt(4)
	v_mul_f32_e32 v48, 0x43000000, v48
	s_waitcnt lgkmcnt(3)
	v_mul_f32_e32 v24, 0x43000000, v50
	v_med3_f32 v26, v48, s35, v84
	v_med3_f32 v24, v24, s35, v84
	ds_read2_b32 v[58:59], v85 offset0:239 offset1:255
	v_cvt_pk_fp8_f32 v96, v26, v24 op_sel:[0,0,1]
	s_waitcnt lgkmcnt(3)
	v_mul_f32_e32 v24, 0x43000000, v52
	s_waitcnt lgkmcnt(2)
	v_mul_f32_e32 v26, 0x43000000, v54
	v_med3_f32 v24, v24, s35, v84
	v_med3_f32 v26, v26, s35, v84
	v_cvt_pk_fp8_f32 v97, v24, v26
	s_waitcnt lgkmcnt(1)
	v_mul_f32_e32 v28, 0x43000000, v56
	s_waitcnt lgkmcnt(0)
	v_mul_f32_e32 v24, 0x43000000, v58
	v_med3_f32 v26, v28, s35, v84
	v_med3_f32 v24, v24, s35, v84
	v_cvt_pk_fp8_f32 v97, v26, v24 op_sel:[0,0,1]
	v_or_b32_e32 v24, s7, v63
	v_mul_u32_u24_e32 v60, 0x2b00, v24
	v_mul_f32_e32 v24, 0x43000000, v25
	v_mul_f32_e32 v25, 0x43000000, v27
	v_med3_f32 v27, v24, s35, v84
	v_med3_f32 v25, v25, s35, v84
	v_mov_b32_e32 v24, v3
	v_cvt_pk_fp8_f32 v24, v27, v25
	v_mul_f32_e32 v26, 0x43000000, v29
	v_mul_f32_e32 v25, 0x43000000, v31
	v_med3_f32 v26, v26, s35, v84
	v_med3_f32 v25, v25, s35, v84
	v_cvt_pk_fp8_f32 v24, v26, v25 op_sel:[0,0,1]
	v_mul_f32_e32 v25, 0x43000000, v37
	v_mul_f32_e32 v26, 0x43000000, v39
	v_med3_f32 v28, v25, s35, v84
	v_med3_f32 v26, v26, s35, v84
	v_mov_b32_e32 v25, v3
	v_cvt_pk_fp8_f32 v25, v28, v26
	v_mul_f32_e32 v27, 0x43000000, v41
	v_mul_f32_e32 v26, 0x43000000, v43
	v_med3_f32 v27, v27, s35, v84
	v_med3_f32 v26, v26, s35, v84
	v_cvt_pk_fp8_f32 v25, v27, v26 op_sel:[0,0,1]
	v_mul_f32_e32 v26, 0x43000000, v45
	v_mul_f32_e32 v27, 0x43000000, v47
	v_med3_f32 v29, v26, s35, v84
	v_med3_f32 v27, v27, s35, v84
	v_mov_b32_e32 v26, v3
	v_cvt_pk_fp8_f32 v26, v29, v27
	v_mul_f32_e32 v28, 0x43000000, v49
	v_mul_f32_e32 v27, 0x43000000, v51
	v_med3_f32 v28, v28, s35, v84
	v_med3_f32 v27, v27, s35, v84
	v_cvt_pk_fp8_f32 v26, v28, v27 op_sel:[0,0,1]
	v_mul_f32_e32 v27, 0x43000000, v53
	v_mul_f32_e32 v28, 0x43000000, v55
	v_med3_f32 v30, v27, s35, v84
	v_med3_f32 v28, v28, s35, v84
	v_mov_b32_e32 v27, v3
	v_cvt_pk_fp8_f32 v27, v30, v28
	v_mul_f32_e32 v29, 0x43000000, v57
	v_mul_f32_e32 v28, 0x43000000, v59
	v_med3_f32 v29, v29, s35, v84
	v_med3_f32 v28, v28, s35, v84
	v_cvt_pk_fp8_f32 v27, v29, v28 op_sel:[0,0,1]
	v_or_b32_e32 v28, s7, v65
	v_mul_u32_u24_e32 v28, 0x2b00, v28
	v_mov_b32_e32 v29, v3
	v_lshl_add_u64 v[60:61], v[32:33], 0, v[60:61]
	v_lshl_add_u64 v[28:29], v[32:33], 0, v[28:29]
	global_store_dwordx4 v[60:61], v[94:97], off
	global_store_dwordx4 v[28:29], v[24:27], off
	s_waitcnt lgkmcnt(0)
	s_branch .LBB0_87

.LBB0_131:
	s_andn2_b64 vcc, exec, s[0:1]
	s_cbranch_vccnz .LBB0_133
	s_add_i32 s0, s3, 0xaa00
	s_and_b32 s1, s0, 0xffff
	s_mul_i32 s1, s1, 0xbe83
	s_lshr_b32 s1, s1, 24
	s_mul_i32 s7, s1, 0x158
	s_sub_i32 s0, s0, s7
	s_lshl_b32 s10, s1, 6
	v_mov_b32_e32 v24, s0
	v_pk_lshlrev_b16 v60, s52, v24 op_sel_hi:[1,0]
	v_or_b32_e32 v24, s10, v35
	v_mul_u32_u24_e32 v24, 0x2b00, v24
	v_readlane_b32 s36, v247, 6
	v_and_b32_e32 v61, 0x7fe0, v60
	v_lshlrev_b32_e32 v24, 2, v24
	v_mov_b32_e32 v25, v3
	v_readlane_b32 s48, v247, 18
	v_readlane_b32 s49, v247, 19
	v_lshlrev_b32_e32 v26, 2, v61
	v_mov_b32_e32 v27, v3
	v_lshl_add_u64 v[24:25], s[48:49], 0, v[24:25]
	v_lshl_add_u64 v[24:25], v[24:25], 0, v[26:27]
	v_lshl_add_u64 v[32:33], v[24:25], 0, v[2:3]
	v_add_co_u32_e32 v28, vcc, s53, v32
	v_readfirstlane_b32 s0, v60
	s_nop 0
	v_addc_co_u32_e32 v29, vcc, 0, v33, vcc
	v_add_co_u32_e32 v36, vcc, s54, v32
	s_nop 0
	v_addc_co_u32_e32 v37, vcc, 0, v33, vcc
	v_add_co_u32_e32 v40, vcc, s55, v32
	s_and_b32 s0, s0, 0x7f000060
	s_nop 0
	v_addc_co_u32_e32 v41, vcc, 0, v33, vcc
	v_add_co_u32_e32 v44, vcc, s56, v32
	s_nop 0
	v_addc_co_u32_e32 v45, vcc, 0, v33, vcc
	v_add_co_u32_e32 v48, vcc, s57, v32
	s_lshr_b32 s1, s0, 16
	s_nop 0
	v_addc_co_u32_e32 v49, vcc, 0, v33, vcc
	s_nop 0
	v_add_co_u32_e32 v52, vcc, s58, v32
	s_or_b32 s0, s0, s1
	s_nop 0
	v_addc_co_u32_e32 v53, vcc, 0, v33, vcc
	v_add_co_u32_e32 v32, vcc, s59, v32
	s_bitset1_b32 s0, 7
	s_nop 0
	v_addc_co_u32_e32 v33, vcc, 0, v33, vcc
	v_or_b32_e32 v32, v63, v61
	v_lshlrev_b32_e32 v32, 2, v32
	s_and_b32 s0, s0, 0xffff
	v_readlane_b32 s37, v247, 7
	v_readlane_b32 s38, v247, 8
	v_readlane_b32 s39, v247, 9
	v_readlane_b32 s40, v247, 10
	v_readlane_b32 s41, v247, 11
	v_readlane_b32 s42, v247, 12
	v_readlane_b32 s43, v247, 13
	v_readlane_b32 s44, v247, 14
	v_readlane_b32 s45, v247, 15
	v_readlane_b32 s46, v247, 16
	v_readlane_b32 s47, v247, 17
	v_readlane_b32 s50, v247, 20
	v_readlane_b32 s51, v247, 21
	s_waitcnt lgkmcnt(0)
	v_mov_b32_e32 v26, v234
	v_or_b32_e32 v27, v65, v61
	v_lshlrev_b32_e32 v27, 2, v27
	ds_read2_b32 v[32:33], v64 offset1:16
	ds_read2_b32 v[36:37], v64 offset0:33 offset1:49
	ds_read2_b32 v[38:39], v64 offset0:66 offset1:82
	ds_read2_b32 v[40:41], v64 offset0:99 offset1:115
	ds_read2_b32 v[42:43], v64 offset0:132 offset1:148
	ds_read2_b32 v[44:45], v64 offset0:165 offset1:181
	ds_read2_b32 v[46:47], v64 offset0:198 offset1:214
	ds_read2_b32 v[48:49], v64 offset0:231 offset1:247
	ds_read2_b32 v[50:51], v85 offset0:8 offset1:24
	ds_read2_b32 v[52:53], v85 offset0:41 offset1:57
	ds_read2_b32 v[54:55], v85 offset0:74 offset1:90
	ds_read2_b32 v[56:57], v85 offset0:107 offset1:123
	ds_read2_b32 v[58:59], v85 offset0:140 offset1:156
	ds_read2_b32 v[60:61], v85 offset0:173 offset1:189
	ds_read2_b32 v[88:89], v85 offset0:206 offset1:222
	v_mov_b32_e32 v87, v235
	v_or_b32_e32 v28, s0, v63
	v_lshlrev_b32_e32 v30, 12, v28
	ds_read2_b32 v[94:95], v85 offset0:239 offset1:255
	v_lshl_add_u64 v[24:25], v[22:23], 0, s[10:11]
	v_div_scale_f32 v27, s[12:13], v26, v26, s61
	v_rcp_f32_e32 v28, v27
	v_div_scale_f32 v29, vcc, s61, v26, s61
	v_fma_f32 v31, -v27, v28, 1.0
	v_fmac_f32_e32 v28, v31, v28
	v_mul_f32_e32 v31, v29, v28
	v_fma_f32 v91, -v27, v31, v29
	v_fmac_f32_e32 v31, v91, v28
	v_fma_f32 v27, -v27, v31, v29
	v_div_fmas_f32 v27, v27, v28, v31
	v_div_fixup_f32 v27, v27, v26, s61
	v_cmp_lt_f32_e32 vcc, 0, v26
	s_nop 1
	v_cndmask_b32_e32 v26, 0, v27, vcc
	s_waitcnt lgkmcnt(14)
	v_mul_f32_e32 v28, v36, v26
	s_waitcnt lgkmcnt(13)
	v_mul_f32_e32 v29, v26, v38
	s_waitcnt lgkmcnt(10)
	v_mul_f32_e32 v36, v26, v44
	s_waitcnt lgkmcnt(9)
	v_mul_f32_e32 v38, v26, v46
	s_waitcnt lgkmcnt(6)
	v_mul_f32_e32 v44, v26, v52
	s_waitcnt lgkmcnt(5)
	v_mul_f32_e32 v46, v26, v54
	s_waitcnt lgkmcnt(2)
	v_mul_f32_e32 v52, v26, v60
	v_mul_f32_e32 v27, v32, v26
	v_mul_f32_e32 v32, v26, v42
	v_mul_f32_e32 v42, v26, v50
	v_mul_f32_e32 v50, v26, v58
	s_waitcnt lgkmcnt(1)
	v_mul_f32_e32 v54, v26, v88
	v_med3_f32 v28, v28, s62, v86
	v_med3_f32 v29, v29, s62, v86
	v_med3_f32 v36, v36, s62, v86
	v_med3_f32 v38, v38, s62, v86
	v_med3_f32 v44, v44, s62, v86
	v_med3_f32 v46, v46, s62, v86
	v_med3_f32 v52, v52, s62, v86
	v_mul_f32_e32 v31, v26, v40
	v_mul_f32_e32 v40, v26, v48
	v_mul_f32_e32 v48, v26, v56
	s_waitcnt lgkmcnt(0)
	v_mul_f32_e32 v26, v26, v94
	v_med3_f32 v27, v27, s62, v86
	v_med3_f32 v32, v32, s62, v86
	v_med3_f32 v42, v42, s62, v86
	v_med3_f32 v50, v50, s62, v86
	v_med3_f32 v54, v54, s62, v86
	v_rndne_f32_e32 v28, v28
	v_rndne_f32_e32 v29, v29
	v_rndne_f32_e32 v36, v36
	v_rndne_f32_e32 v38, v38
	v_rndne_f32_e32 v44, v44
	v_rndne_f32_e32 v46, v46
	v_rndne_f32_e32 v52, v52
	v_med3_f32 v31, v31, s62, v86
	v_med3_f32 v48, v48, s62, v86
	v_med3_f32 v26, v26, s62, v86
	v_rndne_f32_e32 v27, v27
	v_rndne_f32_e32 v32, v32
	v_rndne_f32_e32 v42, v42
	v_rndne_f32_e32 v50, v50
	v_rndne_f32_e32 v54, v54
	v_cvt_i32_f32_e32 v28, v28
	v_cvt_i32_f32_sdwa v29, v29 dst_sel:WORD_1 dst_unused:UNUSED_PAD src0_sel:DWORD
	v_cvt_i32_f32_e32 v36, v36
	v_cvt_i32_f32_sdwa v38, v38 dst_sel:WORD_1 dst_unused:UNUSED_PAD src0_sel:DWORD
	v_cvt_i32_f32_e32 v44, v44
	v_cvt_i32_f32_sdwa v46, v46 dst_sel:WORD_1 dst_unused:UNUSED_PAD src0_sel:DWORD
	v_cvt_i32_f32_e32 v52, v52
	v_med3_f32 v40, v40, s62, v86
	v_rndne_f32_e32 v31, v31
	v_rndne_f32_e32 v48, v48
	v_rndne_f32_e32 v26, v26
	v_cvt_i32_f32_e32 v27, v27
	v_cvt_i32_f32_e32 v32, v32
	v_cvt_i32_f32_e32 v42, v42
	v_cvt_i32_f32_e32 v50, v50
	v_cvt_i32_f32_sdwa v54, v54 dst_sel:WORD_1 dst_unused:UNUSED_PAD src0_sel:DWORD
	v_rndne_f32_e32 v40, v40
	v_cvt_i32_f32_sdwa v31, v31 dst_sel:BYTE_3 dst_unused:UNUSED_PAD src0_sel:DWORD
	v_cvt_i32_f32_sdwa v48, v48 dst_sel:BYTE_3 dst_unused:UNUSED_PAD src0_sel:DWORD
	v_cvt_i32_f32_sdwa v56, v26 dst_sel:BYTE_3 dst_unused:UNUSED_PAD src0_sel:DWORD
	v_cvt_i32_f32_sdwa v40, v40 dst_sel:BYTE_3 dst_unused:UNUSED_PAD src0_sel:DWORD
	v_lshlrev_b32_e32 v26, 8, v28
	v_and_b32_e32 v28, 0xff0000, v29
	v_lshlrev_b32_e32 v29, 8, v36
	v_and_b32_e32 v36, 0xff0000, v38
	v_lshlrev_b32_e32 v38, 8, v44
	v_and_b32_e32 v44, 0xff0000, v46
	v_lshlrev_b32_e32 v46, 8, v52
	v_and_b32_e32 v52, 0xff0000, v54
	v_perm_b32 v26, v26, v27, s63
	v_perm_b32 v27, v29, v32, s63
	v_perm_b32 v29, v38, v42, s63
	v_perm_b32 v32, v46, v50, s63
	v_or3_b32 v26, v26, v28, v31
	v_or3_b32 v28, v29, v44, v48
	v_or3_b32 v29, v32, v52, v56
	v_div_scale_f32 v32, s[12:13], v87, v87, s61
	v_or3_b32 v27, v27, v36, v40
	v_rcp_f32_e32 v36, v32
	v_mov_b32_e32 v31, v3
	v_lshl_add_u64 v[30:31], v[24:25], 0, v[30:31]
	global_store_dwordx4 v[30:31], v[26:29], off
	s_nop 1
	v_fma_f32 v26, -v32, v36, 1.0
	v_fmac_f32_e32 v36, v26, v36
	v_div_scale_f32 v26, vcc, s61, v87, s61
	v_mul_f32_e32 v27, v26, v36
	v_fma_f32 v28, -v32, v27, v26
	v_fmac_f32_e32 v27, v28, v36
	v_fma_f32 v26, -v32, v27, v26
	v_div_fmas_f32 v26, v26, v36, v27
	v_div_fixup_f32 v26, v26, v87, s61
	v_cmp_lt_f32_e32 vcc, 0, v87
	s_nop 1
	v_cndmask_b32_e32 v29, 0, v26, vcc
	v_mul_f32_e32 v27, v37, v29
	v_mul_f32_e32 v26, v33, v29
	v_mul_f32_e32 v28, v29, v39
	v_med3_f32 v27, v27, s62, v86
	v_mul_f32_e32 v30, v29, v41
	v_med3_f32 v26, v26, s62, v86
	v_rndne_f32_e32 v27, v27
	v_med3_f32 v28, v28, s62, v86
	v_rndne_f32_e32 v26, v26
	v_cvt_i32_f32_e32 v27, v27
	v_rndne_f32_e32 v28, v28
	v_med3_f32 v30, v30, s62, v86
	v_cvt_i32_f32_e32 v26, v26
	v_cvt_i32_f32_sdwa v28, v28 dst_sel:WORD_1 dst_unused:UNUSED_PAD src0_sel:DWORD
	v_rndne_f32_e32 v30, v30
	v_cvt_i32_f32_sdwa v30, v30 dst_sel:BYTE_3 dst_unused:UNUSED_PAD src0_sel:DWORD
	v_lshlrev_b32_e32 v27, 8, v27
	v_perm_b32 v26, v27, v26, s63
	v_and_b32_e32 v27, 0xff0000, v28
	v_mul_f32_e32 v28, v29, v45
	v_or3_b32 v26, v26, v27, v30
	v_mul_f32_e32 v27, v29, v43
	v_mul_f32_e32 v30, v29, v47
	v_med3_f32 v28, v28, s62, v86
	v_mul_f32_e32 v31, v29, v49
	v_med3_f32 v27, v27, s62, v86
	v_rndne_f32_e32 v28, v28
	v_med3_f32 v30, v30, s62, v86
	v_rndne_f32_e32 v27, v27
	v_cvt_i32_f32_e32 v28, v28
	v_rndne_f32_e32 v30, v30
	v_med3_f32 v31, v31, s62, v86
	v_cvt_i32_f32_e32 v27, v27
	v_cvt_i32_f32_sdwa v30, v30 dst_sel:WORD_1 dst_unused:UNUSED_PAD src0_sel:DWORD
	v_rndne_f32_e32 v31, v31
	v_cvt_i32_f32_sdwa v31, v31 dst_sel:BYTE_3 dst_unused:UNUSED_PAD src0_sel:DWORD
	v_lshlrev_b32_e32 v28, 8, v28
	v_perm_b32 v27, v28, v27, s63
	v_and_b32_e32 v28, 0xff0000, v30
	v_mul_f32_e32 v30, v29, v53
	v_or3_b32 v27, v27, v28, v31
	v_mul_f32_e32 v28, v29, v51
	v_mul_f32_e32 v31, v29, v55
	v_med3_f32 v30, v30, s62, v86
	v_mul_f32_e32 v32, v29, v57
	v_med3_f32 v28, v28, s62, v86
	v_rndne_f32_e32 v30, v30
	v_med3_f32 v31, v31, s62, v86
	v_rndne_f32_e32 v28, v28
	v_cvt_i32_f32_e32 v30, v30
	v_rndne_f32_e32 v31, v31
	v_med3_f32 v32, v32, s62, v86
	v_cvt_i32_f32_e32 v28, v28
	v_cvt_i32_f32_sdwa v31, v31 dst_sel:WORD_1 dst_unused:UNUSED_PAD src0_sel:DWORD
	v_rndne_f32_e32 v32, v32
	v_cvt_i32_f32_sdwa v32, v32 dst_sel:BYTE_3 dst_unused:UNUSED_PAD src0_sel:DWORD
	v_lshlrev_b32_e32 v30, 8, v30
	v_perm_b32 v28, v30, v28, s63
	v_and_b32_e32 v30, 0xff0000, v31
	v_mul_f32_e32 v31, v29, v61
	v_or3_b32 v28, v28, v30, v32
	v_mul_f32_e32 v30, v29, v59
	v_mul_f32_e32 v32, v29, v89
	v_med3_f32 v31, v31, s62, v86
	v_mul_f32_e32 v29, v29, v95
	v_med3_f32 v30, v30, s62, v86
	v_rndne_f32_e32 v31, v31
	v_med3_f32 v32, v32, s62, v86
	v_rndne_f32_e32 v30, v30
	v_cvt_i32_f32_e32 v31, v31
	v_rndne_f32_e32 v32, v32
	v_med3_f32 v29, v29, s62, v86
	v_cvt_i32_f32_e32 v30, v30
	v_cvt_i32_f32_sdwa v32, v32 dst_sel:WORD_1 dst_unused:UNUSED_PAD src0_sel:DWORD
	v_rndne_f32_e32 v29, v29
	v_cvt_i32_f32_sdwa v29, v29 dst_sel:BYTE_3 dst_unused:UNUSED_PAD src0_sel:DWORD
	v_lshlrev_b32_e32 v31, 8, v31
	v_perm_b32 v30, v31, v30, s63
	v_and_b32_e32 v31, 0xff0000, v32
	v_or3_b32 v29, v30, v31, v29
	v_or_b32_e32 v30, s0, v65
	v_lshlrev_b32_e32 v30, 12, v30
	v_mov_b32_e32 v31, v3
	v_lshl_add_u64 v[24:25], v[24:25], 0, v[30:31]
	global_store_dwordx4 v[24:25], v[26:29], off
	s_waitcnt lgkmcnt(0)
	s_branch .LBB0_87

.LBB0_915:
	v_max3_f32 v127, v114, s41, v115
	v_max3_f32 v129, v138, s41, v139
	v_max3_f32 v127, v127, v116, v117
	v_max3_f32 v129, v129, v140, v141
	v_max3_f32 v127, v127, v118, v119
	v_max3_f32 v129, v129, v146, v147
	v_max3_f32 v127, v127, v120, v121
	v_max3_f32 v129, v129, v148, v149
	v_max3_f32 v127, v127, v122, v123
	v_max3_f32 v129, v129, v154, v155
	v_max3_f32 v127, v127, v124, v125
	v_max3_f32 v129, v129, v156, v157
	v_max3_f32 v127, v127, v130, v131
	v_max3_f32 v129, v129, v162, v163
	v_max3_f32 v127, v127, v132, v133
	v_max3_f32 v129, v129, v164, v165
	v_mov_b32_e32 v227, v127
	v_mov_b32_e32 v228, v127
	v_mov_b32_e32 v229, v129
	v_mov_b32_e32 v230, v129
	s_nop 1
	v_permlane16_swap_b32 v227, v228
	v_permlane16_swap_b32 v229, v230
	s_nop 1
	v_max_f32_e32 v127, v227, v228
	v_max_f32_e32 v129, v229, v230
	v_mov_b32_e32 v227, v127
	v_mov_b32_e32 v228, v127
	v_mov_b32_e32 v229, v129
	v_mov_b32_e32 v230, v129
	s_nop 1
	v_permlane32_swap_b32 v227, v228
	v_permlane32_swap_b32 v229, v230
	s_nop 1
	v_max_f32_e32 v127, v227, v228
	v_max_f32_e32 v129, v229, v230
	v_mov_b32_e32 v126, v129
	v_add_f32_e32 v128, 0x41000000, v226
	v_cmp_gt_f32_e32 vcc, v127, v128
	v_add_f32_e32 v128, 0x41000000, v225
	v_cmp_gt_f32_e64 s[4:5], v126, v128
	s_or_b64 vcc, vcc, s[4:5]
	s_cbranch_vccz .LBB0_917
	v_max_f32_e32 v127, v127, v127
	v_max_f32_e32 v128, v226, v226
	v_max_f32_e32 v129, v128, v127
	v_cmp_neq_f32_e32 vcc, s41, v129
	v_max_f32_e32 v126, v126, v126
	s_nop 0
	v_cndmask_b32_e32 v127, 0, v129, vcc
	v_sub_f32_e32 v127, v226, v127
	v_exp_f32_e32 v128, v127
	v_max_f32_e32 v127, v225, v225
	v_max_f32_e32 v134, v127, v126
	v_cmp_neq_f32_e32 vcc, s41, v134
	v_mov_b32_e32 v127, v128
	v_pk_mul_f32 v[112:113], v[112:113], v[128:129] op_sel_hi:[1,0]
	v_cndmask_b32_e32 v126, 0, v134, vcc
	v_sub_f32_e32 v126, v225, v126
	v_exp_f32_e32 v126, v126
	v_pk_mul_f32 v[110:111], v[110:111], v[128:129] op_sel_hi:[1,0]
	v_pk_mul_f32 v[108:109], v[108:109], v[128:129] op_sel_hi:[1,0]
	v_pk_mul_f32 v[106:107], v[106:107], v[128:129] op_sel_hi:[1,0]
	v_pk_mul_f32 v[104:105], v[104:105], v[128:129] op_sel_hi:[1,0]
	v_pk_mul_f32 v[102:103], v[102:103], v[128:129] op_sel_hi:[1,0]
	v_pk_mul_f32 v[100:101], v[100:101], v[128:129] op_sel_hi:[1,0]
	v_pk_mul_f32 v[98:99], v[98:99], v[128:129] op_sel_hi:[1,0]
	v_pk_mul_f32 v[96:97], v[96:97], v[128:129] op_sel_hi:[1,0]
	v_pk_mul_f32 v[94:95], v[94:95], v[128:129] op_sel_hi:[1,0]
	v_pk_mul_f32 v[92:93], v[92:93], v[128:129] op_sel_hi:[1,0]
	v_pk_mul_f32 v[90:91], v[90:91], v[128:129] op_sel_hi:[1,0]
	v_pk_mul_f32 v[88:89], v[88:89], v[128:129] op_sel_hi:[1,0]
	v_pk_mul_f32 v[86:87], v[86:87], v[128:129] op_sel_hi:[1,0]
	v_pk_mul_f32 v[84:85], v[84:85], v[128:129] op_sel_hi:[1,0]
	v_pk_mul_f32 v[82:83], v[82:83], v[128:129] op_sel_hi:[1,0]
	v_pk_mul_f32 v[194:195], v[194:195], v[126:127]
	v_pk_mul_f32 v[80:81], v[80:81], v[126:127] op_sel_hi:[1,0]
	v_pk_mul_f32 v[78:79], v[78:79], v[126:127] op_sel_hi:[1,0]
	v_pk_mul_f32 v[76:77], v[76:77], v[126:127] op_sel_hi:[1,0]
	v_pk_mul_f32 v[74:75], v[74:75], v[126:127] op_sel_hi:[1,0]
	v_pk_mul_f32 v[72:73], v[72:73], v[126:127] op_sel_hi:[1,0]
	v_pk_mul_f32 v[70:71], v[70:71], v[126:127] op_sel_hi:[1,0]
	v_pk_mul_f32 v[68:69], v[68:69], v[126:127] op_sel_hi:[1,0]
	v_pk_mul_f32 v[66:67], v[66:67], v[126:127] op_sel_hi:[1,0]
	v_pk_mul_f32 v[64:65], v[64:65], v[126:127] op_sel_hi:[1,0]
	v_pk_mul_f32 v[62:63], v[62:63], v[126:127] op_sel_hi:[1,0]
	v_pk_mul_f32 v[60:61], v[60:61], v[126:127] op_sel_hi:[1,0]
	v_pk_mul_f32 v[58:59], v[58:59], v[126:127] op_sel_hi:[1,0]
	v_pk_mul_f32 v[56:57], v[56:57], v[126:127] op_sel_hi:[1,0]
	v_pk_mul_f32 v[54:55], v[54:55], v[126:127] op_sel_hi:[1,0]
	v_pk_mul_f32 v[52:53], v[52:53], v[126:127] op_sel_hi:[1,0]
	v_pk_mul_f32 v[50:51], v[50:51], v[126:127] op_sel_hi:[1,0]
	v_mov_b32_e32 v225, v134
	v_mov_b32_e32 v226, v129
